# GEMM K-loops: B0 fragment LDS reads moved from the head of each K-step into the previous K-step's read-free memory block (covering vmcnt(10) one block earlier), balancing LDS reads per phase 8/4/8/4 i
# speedup vs baseline: 1.0267x; 1.0024x over previous
.LBB0_235:
	s_ashr_i32 s21, s20, 31
	v_cmp_lt_i64_e32 vcc, s[22:23], v[142:143]
	s_lshl_b64 s[22:23], s[20:21], 20
	s_add_u32 s22, s41, s22
	s_addc_u32 s23, s44, s23
	s_and_b64 s[24:25], vcc, exec
	s_cselect_b32 s7, s23, s29
	s_cselect_b32 s21, s22, s28
	s_ashr_i32 s19, s18, 31
	s_lshl_b64 s[24:25], s[18:19], 20
	s_add_u32 s24, s45, s24
	s_addc_u32 s25, s52, s25
	s_and_b64 s[34:35], vcc, exec
	s_cselect_b32 s19, s25, s31
	s_cselect_b32 s72, s24, s30
	s_add_u32 s28, s28, 0x80080
	s_addc_u32 s29, s29, 0
	s_add_u32 s73, s30, 0x100
	v_mov_b32_e32 v2, 0
	s_addc_u32 s74, s31, 0
	s_mov_b32 s75, -2
	v_mov_b32_e32 v3, v2
	v_mov_b32_e32 v4, v2
	v_mov_b32_e32 v5, v2
	v_mov_b32_e32 v6, v2
	v_mov_b32_e32 v7, v2
	v_mov_b32_e32 v8, v2
	v_mov_b32_e32 v9, v2
	v_mov_b32_e32 v18, v2
	v_mov_b32_e32 v19, v2
	v_mov_b32_e32 v20, v2
	v_mov_b32_e32 v21, v2
	v_mov_b32_e32 v22, v2
	v_mov_b32_e32 v23, v2
	v_mov_b32_e32 v24, v2
	v_mov_b32_e32 v25, v2
	v_mov_b32_e32 v34, v2
	v_mov_b32_e32 v35, v2
	v_mov_b32_e32 v36, v2
	v_mov_b32_e32 v37, v2
	v_mov_b32_e32 v38, v2
	v_mov_b32_e32 v39, v2
	v_mov_b32_e32 v40, v2
	v_mov_b32_e32 v41, v2
	v_mov_b32_e32 v50, v2
	v_mov_b32_e32 v51, v2
	v_mov_b32_e32 v52, v2
	v_mov_b32_e32 v53, v2
	v_mov_b32_e32 v54, v2
	v_mov_b32_e32 v55, v2
	v_mov_b32_e32 v56, v2
	v_mov_b32_e32 v57, v2
	v_mov_b32_e32 v10, v2
	v_mov_b32_e32 v11, v2
	v_mov_b32_e32 v12, v2
	v_mov_b32_e32 v13, v2
	v_mov_b32_e32 v14, v2
	v_mov_b32_e32 v15, v2
	v_mov_b32_e32 v16, v2
	v_mov_b32_e32 v17, v2
	v_mov_b32_e32 v26, v2
	v_mov_b32_e32 v27, v2
	v_mov_b32_e32 v28, v2
	v_mov_b32_e32 v29, v2
	v_mov_b32_e32 v30, v2
	v_mov_b32_e32 v31, v2
	v_mov_b32_e32 v32, v2
	v_mov_b32_e32 v33, v2
	v_mov_b32_e32 v42, v2
	v_mov_b32_e32 v43, v2
	v_mov_b32_e32 v44, v2
	v_mov_b32_e32 v45, v2
	v_mov_b32_e32 v46, v2
	v_mov_b32_e32 v47, v2
	v_mov_b32_e32 v48, v2
	v_mov_b32_e32 v49, v2
	v_mov_b32_e32 v58, v2
	v_mov_b32_e32 v59, v2
	v_mov_b32_e32 v60, v2
	v_mov_b32_e32 v61, v2
	v_mov_b32_e32 v62, v2
	v_mov_b32_e32 v63, v2
	v_mov_b32_e32 v64, v2
	v_mov_b32_e32 v65, v2
	v_mov_b32_e32 v66, v2
	v_mov_b32_e32 v67, v2
	v_mov_b32_e32 v68, v2
	v_mov_b32_e32 v69, v2
	v_mov_b32_e32 v70, v2
	v_mov_b32_e32 v71, v2
	v_mov_b32_e32 v72, v2
	v_mov_b32_e32 v73, v2
	v_mov_b32_e32 v82, v2
	v_mov_b32_e32 v83, v2
	v_mov_b32_e32 v84, v2
	v_mov_b32_e32 v85, v2
	v_mov_b32_e32 v86, v2
	v_mov_b32_e32 v87, v2
	v_mov_b32_e32 v88, v2
	v_mov_b32_e32 v89, v2
	v_mov_b32_e32 v98, v2
	v_mov_b32_e32 v99, v2
	v_mov_b32_e32 v100, v2
	v_mov_b32_e32 v101, v2
	v_mov_b32_e32 v102, v2
	v_mov_b32_e32 v103, v2
	v_mov_b32_e32 v104, v2
	v_mov_b32_e32 v105, v2
	v_mov_b32_e32 v114, v2
	v_mov_b32_e32 v115, v2
	v_mov_b32_e32 v116, v2
	v_mov_b32_e32 v117, v2
	v_mov_b32_e32 v118, v2
	v_mov_b32_e32 v119, v2
	v_mov_b32_e32 v120, v2
	v_mov_b32_e32 v121, v2
	v_mov_b32_e32 v74, v2
	v_mov_b32_e32 v75, v2
	v_mov_b32_e32 v76, v2
	v_mov_b32_e32 v77, v2
	v_mov_b32_e32 v78, v2
	v_mov_b32_e32 v79, v2
	v_mov_b32_e32 v80, v2
	v_mov_b32_e32 v81, v2
	v_mov_b32_e32 v90, v2
	v_mov_b32_e32 v91, v2
	v_mov_b32_e32 v92, v2
	v_mov_b32_e32 v93, v2
	v_mov_b32_e32 v94, v2
	v_mov_b32_e32 v95, v2
	v_mov_b32_e32 v96, v2
	v_mov_b32_e32 v97, v2
	v_mov_b32_e32 v106, v2
	v_mov_b32_e32 v107, v2
	v_mov_b32_e32 v108, v2
	v_mov_b32_e32 v109, v2
	v_mov_b32_e32 v110, v2
	v_mov_b32_e32 v111, v2
	v_mov_b32_e32 v112, v2
	v_mov_b32_e32 v113, v2
	v_mov_b32_e32 v122, v2
	v_mov_b32_e32 v123, v2
	v_mov_b32_e32 v124, v2
	v_mov_b32_e32 v125, v2
	v_mov_b32_e32 v126, v2
	v_mov_b32_e32 v127, v2
	v_mov_b32_e32 v128, v2
	v_mov_b32_e32 v129, v2
	ds_read_b128 v[146:149], v156
	ds_read_b128 v[160:163], v156 offset:1024
	ds_read_b128 v[164:167], v156 offset:2048
	ds_read_b128 v[168:171], v156 offset:3072
.LBB0_236:
	s_add_u32 s30, s28, 0xfff80080
	s_addc_u32 s31, s29, -1
	s_cmp_eq_u32 s75, 28
	s_cselect_b32 s35, s7, s31
	s_cselect_b32 s34, s21, s30
	s_cselect_b32 s31, s19, s74
	s_cselect_b32 s30, s72, s73
	v_lshl_add_u64 v[206:207], s[28:29], 0, v[138:139]
	s_add_i32 m0, s9, 0xc000
	ds_read_b128 v[172:175], v157
	ds_read_b128 v[176:179], v157 offset:1024
	ds_read_b128 v[180:183], v157 offset:2048
	ds_read_b128 v[184:187], v157 offset:3072
	ds_read_b128 v[188:191], v157 offset:4096
	ds_read_b128 v[192:195], v157 offset:5120
	ds_read_b128 v[198:201], v157 offset:6144
	ds_read_b128 v[202:205], v157 offset:7168
	global_load_lds_dwordx4 v[206:207], off
	v_lshl_add_u64 v[206:207], s[28:29], 0, v[140:141]
	s_add_i32 m0, s9, 0xe000
	s_nop 0
	global_load_lds_dwordx4 v[206:207], off
	s_waitcnt lgkmcnt(8)
	s_barrier
	s_waitcnt lgkmcnt(0)
	s_waitcnt lgkmcnt(0)
	v_mfma_f32_16x16x32_bf16 v[126:129], v[146:149], v[172:175], v[126:129]
	v_mfma_f32_16x16x32_bf16 v[122:125], v[164:167], v[172:175], v[122:125]
	v_mfma_f32_16x16x32_bf16 v[110:113], v[146:149], v[180:183], v[110:113]
	v_mfma_f32_16x16x32_bf16 v[106:109], v[164:167], v[180:183], v[106:109]
	v_mfma_f32_16x16x32_bf16 v[94:97], v[146:149], v[188:191], v[94:97]
	v_mfma_f32_16x16x32_bf16 v[90:93], v[164:167], v[188:191], v[90:93]
	v_mfma_f32_16x16x32_bf16 v[78:81], v[146:149], v[198:201], v[78:81]
	v_mfma_f32_16x16x32_bf16 v[74:77], v[164:167], v[198:201], v[74:77]
	v_mfma_f32_16x16x32_bf16 v[126:129], v[160:163], v[176:179], v[126:129]
	v_mfma_f32_16x16x32_bf16 v[122:125], v[168:171], v[176:179], v[122:125]
	v_mfma_f32_16x16x32_bf16 v[110:113], v[160:163], v[184:187], v[110:113]
	v_mfma_f32_16x16x32_bf16 v[106:109], v[168:171], v[184:187], v[106:109]
	v_mfma_f32_16x16x32_bf16 v[94:97], v[160:163], v[192:195], v[94:97]
	v_mfma_f32_16x16x32_bf16 v[90:93], v[168:171], v[192:195], v[90:93]
	v_mfma_f32_16x16x32_bf16 v[78:81], v[160:163], v[202:205], v[78:81]
	v_mfma_f32_16x16x32_bf16 v[74:77], v[168:171], v[202:205], v[74:77]
	s_barrier
	s_add_i32 s76, s69, s40
	v_lshl_add_u64 v[222:223], s[30:31], 0, v[132:133]
	s_mov_b32 m0, s76
	ds_read_b128 v[206:209], v158
	ds_read_b128 v[210:213], v158 offset:1024
	ds_read_b128 v[214:217], v158 offset:2048
	ds_read_b128 v[218:221], v158 offset:3072
	global_load_lds_dwordx4 v[222:223], off
	v_lshl_add_u64 v[224:225], s[30:31], 0, v[136:137]
	s_add_i32 m0, s76, 0x2000
	s_nop 0
	global_load_lds_dwordx4 v[224:225], off
	s_barrier
	s_waitcnt lgkmcnt(0)
	s_waitcnt lgkmcnt(0)
	v_mfma_f32_16x16x32_bf16 v[118:121], v[206:209], v[172:175], v[118:121]
	v_mfma_f32_16x16x32_bf16 v[114:117], v[214:217], v[172:175], v[114:117]
	v_mfma_f32_16x16x32_bf16 v[102:105], v[206:209], v[180:183], v[102:105]
	v_mfma_f32_16x16x32_bf16 v[98:101], v[214:217], v[180:183], v[98:101]
	v_mfma_f32_16x16x32_bf16 v[86:89], v[206:209], v[188:191], v[86:89]
	v_mfma_f32_16x16x32_bf16 v[82:85], v[214:217], v[188:191], v[82:85]
	v_mfma_f32_16x16x32_bf16 v[70:73], v[206:209], v[198:201], v[70:73]
	v_mfma_f32_16x16x32_bf16 v[66:69], v[214:217], v[198:201], v[66:69]
	v_mfma_f32_16x16x32_bf16 v[118:121], v[210:213], v[176:179], v[118:121]
	v_mfma_f32_16x16x32_bf16 v[114:117], v[218:221], v[176:179], v[114:117]
	v_mfma_f32_16x16x32_bf16 v[102:105], v[210:213], v[184:187], v[102:105]
	v_mfma_f32_16x16x32_bf16 v[98:101], v[218:221], v[184:187], v[98:101]
	v_mfma_f32_16x16x32_bf16 v[86:89], v[210:213], v[192:195], v[86:89]
	v_mfma_f32_16x16x32_bf16 v[82:85], v[218:221], v[192:195], v[82:85]
	v_mfma_f32_16x16x32_bf16 v[70:73], v[210:213], v[202:205], v[70:73]
	v_mfma_f32_16x16x32_bf16 v[66:69], v[218:221], v[202:205], v[66:69]
	s_mov_b32 m0, s9
	v_lshl_add_u64 v[226:227], s[34:35], 0, v[130:131]
	s_barrier
	ds_read_b128 v[172:175], v157 offset:16384
	ds_read_b128 v[176:179], v157 offset:17408
	ds_read_b128 v[180:183], v157 offset:18432
	ds_read_b128 v[184:187], v157 offset:19456
	ds_read_b128 v[188:191], v157 offset:20480
	ds_read_b128 v[192:195], v157 offset:21504
	ds_read_b128 v[198:201], v157 offset:22528
	ds_read_b128 v[202:205], v157 offset:23552
	global_load_lds_dwordx4 v[226:227], off
	v_lshl_add_u64 v[228:229], s[34:35], 0, v[134:135]
	s_mov_b32 m0, s53
	s_nop 0
	global_load_lds_dwordx4 v[228:229], off
	s_waitcnt vmcnt(10)
	s_barrier
	s_waitcnt lgkmcnt(0)
	s_waitcnt lgkmcnt(0)
	v_mfma_f32_16x16x32_bf16 v[62:65], v[146:149], v[172:175], v[62:65]
	v_mfma_f32_16x16x32_bf16 v[58:61], v[164:167], v[172:175], v[58:61]
	v_mfma_f32_16x16x32_bf16 v[46:49], v[146:149], v[180:183], v[46:49]
	v_mfma_f32_16x16x32_bf16 v[42:45], v[164:167], v[180:183], v[42:45]
	v_mfma_f32_16x16x32_bf16 v[30:33], v[146:149], v[188:191], v[30:33]
	v_mfma_f32_16x16x32_bf16 v[26:29], v[164:167], v[188:191], v[26:29]
	v_mfma_f32_16x16x32_bf16 v[14:17], v[146:149], v[198:201], v[14:17]
	v_mfma_f32_16x16x32_bf16 v[10:13], v[164:167], v[198:201], v[10:13]
	v_mfma_f32_16x16x32_bf16 v[62:65], v[160:163], v[176:179], v[62:65]
	v_mfma_f32_16x16x32_bf16 v[58:61], v[168:171], v[176:179], v[58:61]
	v_mfma_f32_16x16x32_bf16 v[46:49], v[160:163], v[184:187], v[46:49]
	v_mfma_f32_16x16x32_bf16 v[42:45], v[168:171], v[184:187], v[42:45]
	v_mfma_f32_16x16x32_bf16 v[30:33], v[160:163], v[192:195], v[30:33]
	v_mfma_f32_16x16x32_bf16 v[26:29], v[168:171], v[192:195], v[26:29]
	v_mfma_f32_16x16x32_bf16 v[14:17], v[160:163], v[202:205], v[14:17]
	v_mfma_f32_16x16x32_bf16 v[10:13], v[168:171], v[202:205], v[10:13]
	s_barrier
	ds_read_b128 v[146:149], v156 offset:32768
	ds_read_b128 v[160:163], v156 offset:33792
	ds_read_b128 v[164:167], v156 offset:34816
	ds_read_b128 v[168:171], v156 offset:35840
	s_add_u32 s76, s30, 0x80000
	s_addc_u32 s77, s31, 0
	s_add_i32 s78, s70, s40
	v_lshl_add_u64 v[230:231], s[76:77], 0, v[132:133]
	s_mov_b32 m0, s78
	s_nop 0
	global_load_lds_dwordx4 v[230:231], off
	v_lshl_add_u64 v[230:231], s[76:77], 0, v[136:137]
	s_add_i32 m0, s78, 0x2000
	s_nop 0
	global_load_lds_dwordx4 v[230:231], off
	s_waitcnt vmcnt(6)
	s_barrier
	v_mfma_f32_16x16x32_bf16 v[54:57], v[206:209], v[172:175], v[54:57]
	v_mfma_f32_16x16x32_bf16 v[50:53], v[214:217], v[172:175], v[50:53]
	v_mfma_f32_16x16x32_bf16 v[38:41], v[206:209], v[180:183], v[38:41]
	v_mfma_f32_16x16x32_bf16 v[34:37], v[214:217], v[180:183], v[34:37]
	v_mfma_f32_16x16x32_bf16 v[22:25], v[206:209], v[188:191], v[22:25]
	v_mfma_f32_16x16x32_bf16 v[18:21], v[214:217], v[188:191], v[18:21]
	v_mfma_f32_16x16x32_bf16 v[6:9], v[206:209], v[198:201], v[6:9]
	v_mfma_f32_16x16x32_bf16 v[2:5], v[214:217], v[198:201], v[2:5]
	v_mfma_f32_16x16x32_bf16 v[54:57], v[210:213], v[176:179], v[54:57]
	v_mfma_f32_16x16x32_bf16 v[50:53], v[218:221], v[176:179], v[50:53]
	v_mfma_f32_16x16x32_bf16 v[38:41], v[210:213], v[184:187], v[38:41]
	v_mfma_f32_16x16x32_bf16 v[34:37], v[218:221], v[184:187], v[34:37]
	v_mfma_f32_16x16x32_bf16 v[22:25], v[210:213], v[192:195], v[22:25]
	v_mfma_f32_16x16x32_bf16 v[18:21], v[218:221], v[192:195], v[18:21]
	v_mfma_f32_16x16x32_bf16 v[6:9], v[210:213], v[202:205], v[6:9]
	v_mfma_f32_16x16x32_bf16 v[2:5], v[218:221], v[202:205], v[2:5]
	s_add_i32 s76, 0, 0x18000
	v_add_u32_e32 v159, s76, v153
	s_barrier
	s_add_u32 s34, s34, 0x80000
	s_addc_u32 s35, s35, 0
	s_mov_b32 m0, s54
	v_lshl_add_u64 v[206:207], s[34:35], 0, v[130:131]
	ds_read_b128 v[172:175], v157 offset:32768
	ds_read_b128 v[176:179], v157 offset:33792
	ds_read_b128 v[180:183], v157 offset:34816
	ds_read_b128 v[184:187], v157 offset:35840
	ds_read_b128 v[188:191], v157 offset:36864
	ds_read_b128 v[192:195], v157 offset:37888
	ds_read_b128 v[198:201], v157 offset:38912
	ds_read_b128 v[202:205], v157 offset:39936
	global_load_lds_dwordx4 v[206:207], off
	v_lshl_add_u64 v[206:207], s[34:35], 0, v[134:135]
	s_mov_b32 m0, s55
	s_nop 0
	global_load_lds_dwordx4 v[206:207], off
	s_waitcnt lgkmcnt(8)
	s_barrier
	s_waitcnt lgkmcnt(0)
	s_waitcnt lgkmcnt(0)
	v_mfma_f32_16x16x32_bf16 v[126:129], v[146:149], v[172:175], v[126:129]
	v_mfma_f32_16x16x32_bf16 v[122:125], v[164:167], v[172:175], v[122:125]
	v_mfma_f32_16x16x32_bf16 v[110:113], v[146:149], v[180:183], v[110:113]
	v_mfma_f32_16x16x32_bf16 v[106:109], v[164:167], v[180:183], v[106:109]
	v_mfma_f32_16x16x32_bf16 v[94:97], v[146:149], v[188:191], v[94:97]
	v_mfma_f32_16x16x32_bf16 v[90:93], v[164:167], v[188:191], v[90:93]
	v_mfma_f32_16x16x32_bf16 v[78:81], v[146:149], v[198:201], v[78:81]
	v_mfma_f32_16x16x32_bf16 v[74:77], v[164:167], v[198:201], v[74:77]
	v_mfma_f32_16x16x32_bf16 v[126:129], v[160:163], v[176:179], v[126:129]
	v_mfma_f32_16x16x32_bf16 v[122:125], v[168:171], v[176:179], v[122:125]
	v_mfma_f32_16x16x32_bf16 v[110:113], v[160:163], v[184:187], v[110:113]
	v_mfma_f32_16x16x32_bf16 v[106:109], v[168:171], v[184:187], v[106:109]
	v_mfma_f32_16x16x32_bf16 v[94:97], v[160:163], v[192:195], v[94:97]
	v_mfma_f32_16x16x32_bf16 v[90:93], v[168:171], v[192:195], v[90:93]
	v_mfma_f32_16x16x32_bf16 v[78:81], v[160:163], v[202:205], v[78:81]
	v_mfma_f32_16x16x32_bf16 v[74:77], v[168:171], v[202:205], v[74:77]
	s_barrier
	s_add_i32 s34, 0, 0x1c000
	s_add_i32 s35, s76, s40
	v_add_u32_e32 v159, s34, v153
	v_lshl_add_u64 v[222:223], v[222:223], 0, s[14:15]
	s_mov_b32 m0, s35
	ds_read_b128 v[206:209], v159
	ds_read_b128 v[210:213], v159 offset:1024
	ds_read_b128 v[214:217], v159 offset:2048
	ds_read_b128 v[218:221], v159 offset:3072
	global_load_lds_dwordx4 v[222:223], off
	v_lshl_add_u64 v[222:223], v[224:225], 0, s[14:15]
	s_add_i32 m0, s35, 0x2000
	s_nop 0
	global_load_lds_dwordx4 v[222:223], off
	s_barrier
	s_waitcnt lgkmcnt(0)
	s_waitcnt lgkmcnt(0)
	v_mfma_f32_16x16x32_bf16 v[118:121], v[206:209], v[172:175], v[118:121]
	v_mfma_f32_16x16x32_bf16 v[114:117], v[214:217], v[172:175], v[114:117]
	v_mfma_f32_16x16x32_bf16 v[102:105], v[206:209], v[180:183], v[102:105]
	v_mfma_f32_16x16x32_bf16 v[98:101], v[214:217], v[180:183], v[98:101]
	v_mfma_f32_16x16x32_bf16 v[86:89], v[206:209], v[188:191], v[86:89]
	v_mfma_f32_16x16x32_bf16 v[82:85], v[214:217], v[188:191], v[82:85]
	v_mfma_f32_16x16x32_bf16 v[70:73], v[206:209], v[198:201], v[70:73]
	v_mfma_f32_16x16x32_bf16 v[66:69], v[214:217], v[198:201], v[66:69]
	v_mfma_f32_16x16x32_bf16 v[118:121], v[210:213], v[176:179], v[118:121]
	v_mfma_f32_16x16x32_bf16 v[114:117], v[218:221], v[176:179], v[114:117]
	v_mfma_f32_16x16x32_bf16 v[102:105], v[210:213], v[184:187], v[102:105]
	v_mfma_f32_16x16x32_bf16 v[98:101], v[218:221], v[184:187], v[98:101]
	v_mfma_f32_16x16x32_bf16 v[86:89], v[210:213], v[192:195], v[86:89]
	v_mfma_f32_16x16x32_bf16 v[82:85], v[218:221], v[192:195], v[82:85]
	v_mfma_f32_16x16x32_bf16 v[70:73], v[210:213], v[202:205], v[70:73]
	v_mfma_f32_16x16x32_bf16 v[66:69], v[218:221], v[202:205], v[66:69]
	s_mov_b32 m0, s67
	v_lshl_add_u64 v[222:223], v[226:227], 0, s[14:15]
	s_barrier
	ds_read_b128 v[172:175], v157 offset:49152
	ds_read_b128 v[176:179], v157 offset:50176
	ds_read_b128 v[180:183], v157 offset:51200
	ds_read_b128 v[184:187], v157 offset:52224
	ds_read_b128 v[188:191], v157 offset:53248
	ds_read_b128 v[192:195], v157 offset:54272
	ds_read_b128 v[198:201], v157 offset:55296
	ds_read_b128 v[202:205], v157 offset:56320
	global_load_lds_dwordx4 v[222:223], off
	v_lshl_add_u64 v[222:223], v[228:229], 0, s[14:15]
	s_mov_b32 m0, s68
	s_nop 0
	global_load_lds_dwordx4 v[222:223], off
	s_waitcnt vmcnt(10)
	s_barrier
	s_waitcnt lgkmcnt(0)
	s_waitcnt lgkmcnt(0)
	v_mfma_f32_16x16x32_bf16 v[62:65], v[146:149], v[172:175], v[62:65]
	v_mfma_f32_16x16x32_bf16 v[58:61], v[164:167], v[172:175], v[58:61]
	v_mfma_f32_16x16x32_bf16 v[46:49], v[146:149], v[180:183], v[46:49]
	v_mfma_f32_16x16x32_bf16 v[42:45], v[164:167], v[180:183], v[42:45]
	v_mfma_f32_16x16x32_bf16 v[30:33], v[146:149], v[188:191], v[30:33]
	v_mfma_f32_16x16x32_bf16 v[26:29], v[164:167], v[188:191], v[26:29]
	v_mfma_f32_16x16x32_bf16 v[14:17], v[146:149], v[198:201], v[14:17]
	v_mfma_f32_16x16x32_bf16 v[10:13], v[164:167], v[198:201], v[10:13]
	v_mfma_f32_16x16x32_bf16 v[62:65], v[160:163], v[176:179], v[62:65]
	v_mfma_f32_16x16x32_bf16 v[58:61], v[168:171], v[176:179], v[58:61]
	v_mfma_f32_16x16x32_bf16 v[46:49], v[160:163], v[184:187], v[46:49]
	v_mfma_f32_16x16x32_bf16 v[42:45], v[168:171], v[184:187], v[42:45]
	v_mfma_f32_16x16x32_bf16 v[30:33], v[160:163], v[192:195], v[30:33]
	v_mfma_f32_16x16x32_bf16 v[26:29], v[168:171], v[192:195], v[26:29]
	v_mfma_f32_16x16x32_bf16 v[14:17], v[160:163], v[202:205], v[14:17]
	v_mfma_f32_16x16x32_bf16 v[10:13], v[168:171], v[202:205], v[10:13]
	s_barrier
	ds_read_b128 v[146:149], v156
	ds_read_b128 v[160:163], v156 offset:1024
	ds_read_b128 v[164:167], v156 offset:2048
	ds_read_b128 v[168:171], v156 offset:3072
	s_add_u32 s30, s30, 0x80080
	s_addc_u32 s31, s31, 0
	s_add_i32 s34, s34, s40
	v_lshl_add_u64 v[230:231], s[30:31], 0, v[132:133]
	s_mov_b32 m0, s34
	s_nop 0
	global_load_lds_dwordx4 v[230:231], off
	v_lshl_add_u64 v[230:231], s[30:31], 0, v[136:137]
	s_add_i32 m0, s34, 0x2000
	s_nop 0
	global_load_lds_dwordx4 v[230:231], off
	s_waitcnt vmcnt(6)
	s_barrier
	v_mfma_f32_16x16x32_bf16 v[54:57], v[206:209], v[172:175], v[54:57]
	v_mfma_f32_16x16x32_bf16 v[50:53], v[214:217], v[172:175], v[50:53]
	v_mfma_f32_16x16x32_bf16 v[38:41], v[206:209], v[180:183], v[38:41]
	v_mfma_f32_16x16x32_bf16 v[34:37], v[214:217], v[180:183], v[34:37]
	v_mfma_f32_16x16x32_bf16 v[22:25], v[206:209], v[188:191], v[22:25]
	v_mfma_f32_16x16x32_bf16 v[18:21], v[214:217], v[188:191], v[18:21]
	v_mfma_f32_16x16x32_bf16 v[6:9], v[206:209], v[198:201], v[6:9]
	v_mfma_f32_16x16x32_bf16 v[2:5], v[214:217], v[198:201], v[2:5]
	v_mfma_f32_16x16x32_bf16 v[54:57], v[210:213], v[176:179], v[54:57]
	v_mfma_f32_16x16x32_bf16 v[50:53], v[218:221], v[176:179], v[50:53]
	v_mfma_f32_16x16x32_bf16 v[38:41], v[210:213], v[184:187], v[38:41]
	v_mfma_f32_16x16x32_bf16 v[34:37], v[218:221], v[184:187], v[34:37]
	v_mfma_f32_16x16x32_bf16 v[22:25], v[210:213], v[192:195], v[22:25]
	v_mfma_f32_16x16x32_bf16 v[18:21], v[218:221], v[192:195], v[18:21]
	v_mfma_f32_16x16x32_bf16 v[6:9], v[210:213], v[202:205], v[6:9]
	v_mfma_f32_16x16x32_bf16 v[2:5], v[218:221], v[202:205], v[2:5]
	s_add_i32 s75, s75, 2
	s_add_u32 s28, s28, 0x100
	s_addc_u32 s29, s29, 0
	s_add_u32 s73, s73, 0x100
	s_addc_u32 s74, s74, 0
	s_cmp_gt_u32 s75, 29
	s_barrier
	s_cbranch_scc0 .LBB0_236
	s_waitcnt lgkmcnt(0)
	s_add_i32 s7, s8, -12
	s_cmp_lt_u32 s7, 8
	v_lshl_add_u32 v159, s6, 8, v152
	s_cselect_b64 s[28:29], -1, 0
	s_cmp_lt_i32 s6, 64
	v_lshrrev_b32_e32 v160, 6, v159
	s_cselect_b64 s[30:31], -1, 0
	v_cndmask_b32_e64 v146, v151, v160, s[0:1]
	v_lshlrev_b32_e32 v146, 5, v146
	s_and_b64 s[28:29], s[28:29], s[30:31]
	v_and_b32_e32 v146, 0x7e0, v146
	v_cndmask_b32_e64 v147, 0, 1, s[28:29]
	v_cmp_ne_u32_e64 s[6:7], 1, v147
	s_andn2_b64 vcc, exec, s[28:29]
	v_lshl_add_u32 v161, v146, 2, v154
	s_cbranch_vccnz .LBB0_239
	ds_read_b128 v[146:149], v161
	ds_read_b128 v[162:165], v161 offset:16
	v_mov_b32_e32 v166, v129
	s_cmp_lt_u32 s8, 16
	s_cselect_b64 vcc, -1, 0
	s_waitcnt lgkmcnt(0)
	v_pk_mul_f32 v[168:169], v[126:127], v[146:147] op_sel:[1,1] op_sel_hi:[1,0]
	v_pk_mul_f32 v[166:167], v[166:167], v[148:149] op_sel:[0,1] op_sel_hi:[0,0]
	v_pk_fma_f32 v[170:171], v[126:127], v[146:147], v[168:169] op_sel_hi:[0,1,1] neg_lo:[0,0,1] neg_hi:[0,0,1]
	v_pk_fma_f32 v[126:127], v[126:127], v[146:147], v[168:169] op_sel_hi:[0,1,1]
	v_pk_fma_f32 v[146:147], v[128:129], v[148:149], v[166:167] op_sel_hi:[0,1,1] neg_lo:[0,0,1] neg_hi:[0,0,1]
	v_pk_fma_f32 v[128:129], v[128:129], v[148:149], v[166:167] op_sel_hi:[0,1,1]
	v_pk_mul_f32 v[148:149], v[122:123], v[162:163] op_sel:[1,1] op_sel_hi:[1,0]
	v_mov_b32_e32 v147, v129
	v_pk_fma_f32 v[166:167], v[122:123], v[162:163], v[148:149] op_sel_hi:[0,1,1] neg_lo:[0,0,1] neg_hi:[0,0,1]
	v_pk_fma_f32 v[122:123], v[122:123], v[162:163], v[148:149] op_sel_hi:[0,1,1]
	v_mov_b32_e32 v122, v125
	v_pk_mul_f32 v[148:149], v[122:123], v[164:165] op_sel:[0,1] op_sel_hi:[0,0]
	v_pk_fma_f32 v[162:163], v[124:125], v[164:165], v[148:149] op_sel_hi:[0,1,1] neg_lo:[0,0,1] neg_hi:[0,0,1]
	v_pk_fma_f32 v[124:125], v[124:125], v[164:165], v[148:149] op_sel_hi:[0,1,1]
	v_mov_b32_e32 v171, v127
	v_mov_b32_e32 v163, v125
	v_mov_b32_e32 v167, v123
	v_pk_mul_f32 v[148:149], v[146:147], s[16:17] op_sel_hi:[1,0]
	v_pk_mul_f32 v[164:165], v[170:171], s[16:17] op_sel_hi:[1,0]
	v_pk_mul_f32 v[168:169], v[162:163], s[16:17] op_sel_hi:[1,0]
	v_pk_mul_f32 v[172:173], v[166:167], s[16:17] op_sel_hi:[1,0]
	v_cndmask_b32_e32 v124, v162, v168, vcc
	v_cndmask_b32_e32 v125, v125, v169, vcc
	v_cndmask_b32_e32 v122, v166, v172, vcc
	v_cndmask_b32_e32 v123, v123, v173, vcc
	v_cndmask_b32_e32 v128, v146, v148, vcc
	v_cndmask_b32_e32 v129, v129, v149, vcc
	v_cndmask_b32_e32 v126, v170, v164, vcc
	v_cndmask_b32_e32 v127, v127, v165, vcc

.LBB0_714:
	s_ashr_i32 s21, s20, 31
	v_cmp_lt_i64_e32 vcc, s[22:23], v[142:143]
	s_lshl_b64 s[22:23], s[20:21], 20
	s_add_u32 s22, s36, s22
	s_addc_u32 s23, s37, s23
	s_and_b64 s[24:25], vcc, exec
	s_cselect_b32 s21, s23, s29
	s_cselect_b32 s70, s22, s28
	s_ashr_i32 s19, s18, 31
	s_lshl_b64 s[24:25], s[18:19], 20
	s_add_u32 s24, s38, s24
	s_addc_u32 s25, s39, s25
	s_and_b64 s[34:35], vcc, exec
	s_cselect_b32 s19, s25, s31
	s_cselect_b32 s71, s24, s30
	s_add_u32 s28, s28, 0x80080
	s_addc_u32 s29, s29, 0
	s_add_u32 s72, s30, 0x100
	v_mov_b32_e32 v2, 0
	s_addc_u32 s73, s31, 0
	s_mov_b32 s74, -2
	v_mov_b32_e32 v3, v2
	v_mov_b32_e32 v4, v2
	v_mov_b32_e32 v5, v2
	v_mov_b32_e32 v6, v2
	v_mov_b32_e32 v7, v2
	v_mov_b32_e32 v8, v2
	v_mov_b32_e32 v9, v2
	v_mov_b32_e32 v10, v2
	v_mov_b32_e32 v11, v2
	v_mov_b32_e32 v12, v2
	v_mov_b32_e32 v13, v2
	v_mov_b32_e32 v18, v2
	v_mov_b32_e32 v19, v2
	v_mov_b32_e32 v20, v2
	v_mov_b32_e32 v21, v2
	v_mov_b32_e32 v26, v2
	v_mov_b32_e32 v27, v2
	v_mov_b32_e32 v28, v2
	v_mov_b32_e32 v29, v2
	v_mov_b32_e32 v34, v2
	v_mov_b32_e32 v35, v2
	v_mov_b32_e32 v36, v2
	v_mov_b32_e32 v37, v2
	v_mov_b32_e32 v42, v2
	v_mov_b32_e32 v43, v2
	v_mov_b32_e32 v44, v2
	v_mov_b32_e32 v45, v2
	v_mov_b32_e32 v50, v2
	v_mov_b32_e32 v51, v2
	v_mov_b32_e32 v52, v2
	v_mov_b32_e32 v53, v2
	v_mov_b32_e32 v14, v2
	v_mov_b32_e32 v15, v2
	v_mov_b32_e32 v16, v2
	v_mov_b32_e32 v17, v2
	v_mov_b32_e32 v22, v2
	v_mov_b32_e32 v23, v2
	v_mov_b32_e32 v24, v2
	v_mov_b32_e32 v25, v2
	v_mov_b32_e32 v30, v2
	v_mov_b32_e32 v31, v2
	v_mov_b32_e32 v32, v2
	v_mov_b32_e32 v33, v2
	v_mov_b32_e32 v38, v2
	v_mov_b32_e32 v39, v2
	v_mov_b32_e32 v40, v2
	v_mov_b32_e32 v41, v2
	v_mov_b32_e32 v46, v2
	v_mov_b32_e32 v47, v2
	v_mov_b32_e32 v48, v2
	v_mov_b32_e32 v49, v2
	v_mov_b32_e32 v54, v2
	v_mov_b32_e32 v55, v2
	v_mov_b32_e32 v56, v2
	v_mov_b32_e32 v57, v2
	v_mov_b32_e32 v58, v2
	v_mov_b32_e32 v59, v2
	v_mov_b32_e32 v60, v2
	v_mov_b32_e32 v61, v2
	v_mov_b32_e32 v62, v2
	v_mov_b32_e32 v63, v2
	v_mov_b32_e32 v64, v2
	v_mov_b32_e32 v65, v2
	v_mov_b32_e32 v66, v2
	v_mov_b32_e32 v67, v2
	v_mov_b32_e32 v68, v2
	v_mov_b32_e32 v69, v2
	v_mov_b32_e32 v70, v2
	v_mov_b32_e32 v71, v2
	v_mov_b32_e32 v72, v2
	v_mov_b32_e32 v73, v2
	v_mov_b32_e32 v78, v2
	v_mov_b32_e32 v79, v2
	v_mov_b32_e32 v80, v2
	v_mov_b32_e32 v81, v2
	v_mov_b32_e32 v86, v2
	v_mov_b32_e32 v87, v2
	v_mov_b32_e32 v88, v2
	v_mov_b32_e32 v89, v2
	v_mov_b32_e32 v94, v2
	v_mov_b32_e32 v95, v2
	v_mov_b32_e32 v96, v2
	v_mov_b32_e32 v97, v2
	v_mov_b32_e32 v102, v2
	v_mov_b32_e32 v103, v2
	v_mov_b32_e32 v104, v2
	v_mov_b32_e32 v105, v2
	v_mov_b32_e32 v110, v2
	v_mov_b32_e32 v111, v2
	v_mov_b32_e32 v112, v2
	v_mov_b32_e32 v113, v2
	v_mov_b32_e32 v118, v2
	v_mov_b32_e32 v119, v2
	v_mov_b32_e32 v120, v2
	v_mov_b32_e32 v121, v2
	v_mov_b32_e32 v74, v2
	v_mov_b32_e32 v75, v2
	v_mov_b32_e32 v76, v2
	v_mov_b32_e32 v77, v2
	v_mov_b32_e32 v82, v2
	v_mov_b32_e32 v83, v2
	v_mov_b32_e32 v84, v2
	v_mov_b32_e32 v85, v2
	v_mov_b32_e32 v90, v2
	v_mov_b32_e32 v91, v2
	v_mov_b32_e32 v92, v2
	v_mov_b32_e32 v93, v2
	v_mov_b32_e32 v98, v2
	v_mov_b32_e32 v99, v2
	v_mov_b32_e32 v100, v2
	v_mov_b32_e32 v101, v2
	v_mov_b32_e32 v106, v2
	v_mov_b32_e32 v107, v2
	v_mov_b32_e32 v108, v2
	v_mov_b32_e32 v109, v2
	v_mov_b32_e32 v114, v2
	v_mov_b32_e32 v115, v2
	v_mov_b32_e32 v116, v2
	v_mov_b32_e32 v117, v2
	v_mov_b32_e32 v122, v2
	v_mov_b32_e32 v123, v2
	v_mov_b32_e32 v124, v2
	v_mov_b32_e32 v125, v2
	v_mov_b32_e32 v126, v2
	v_mov_b32_e32 v127, v2
	v_mov_b32_e32 v128, v2
	v_mov_b32_e32 v129, v2
	ds_read_b128 v[154:157], v150
	ds_read_b128 v[158:161], v150 offset:1024
	ds_read_b128 v[162:165], v150 offset:2048
	ds_read_b128 v[166:169], v150 offset:3072
.LBB0_715:
	s_add_u32 s30, s28, 0xfff80080
	s_addc_u32 s31, s29, -1
	s_cmp_eq_u32 s74, 28
	s_cselect_b32 s35, s21, s31
	s_cselect_b32 s34, s70, s30
	s_cselect_b32 s31, s19, s73
	s_cselect_b32 s30, s71, s72
	v_lshl_add_u64 v[146:147], s[28:29], 0, v[138:139]
	s_add_i32 m0, s27, 0xc000
	ds_read_b128 v[170:173], v151
	ds_read_b128 v[174:177], v151 offset:1024
	ds_read_b128 v[178:181], v151 offset:2048
	ds_read_b128 v[182:185], v151 offset:3072
	ds_read_b128 v[186:189], v151 offset:4096
	ds_read_b128 v[190:193], v151 offset:5120
	ds_read_b128 v[198:201], v151 offset:6144
	ds_read_b128 v[202:205], v151 offset:7168
	global_load_lds_dwordx4 v[146:147], off
	v_lshl_add_u64 v[146:147], s[28:29], 0, v[140:141]
	s_add_i32 m0, s27, 0xe000
	s_nop 0
	global_load_lds_dwordx4 v[146:147], off
	s_waitcnt lgkmcnt(8)
	s_barrier
	s_waitcnt lgkmcnt(0)
	s_waitcnt lgkmcnt(0)
	v_mfma_f32_16x16x32_bf16 v[126:129], v[154:157], v[170:173], v[126:129]
	v_mfma_f32_16x16x32_bf16 v[122:125], v[162:165], v[170:173], v[122:125]
	v_mfma_f32_16x16x32_bf16 v[114:117], v[154:157], v[178:181], v[114:117]
	v_mfma_f32_16x16x32_bf16 v[106:109], v[162:165], v[178:181], v[106:109]
	v_mfma_f32_16x16x32_bf16 v[98:101], v[154:157], v[186:189], v[98:101]
	v_mfma_f32_16x16x32_bf16 v[90:93], v[162:165], v[186:189], v[90:93]
	v_mfma_f32_16x16x32_bf16 v[82:85], v[154:157], v[198:201], v[82:85]
	v_mfma_f32_16x16x32_bf16 v[74:77], v[162:165], v[198:201], v[74:77]
	v_mfma_f32_16x16x32_bf16 v[126:129], v[158:161], v[174:177], v[126:129]
	v_mfma_f32_16x16x32_bf16 v[122:125], v[166:169], v[174:177], v[122:125]
	v_mfma_f32_16x16x32_bf16 v[114:117], v[158:161], v[182:185], v[114:117]
	v_mfma_f32_16x16x32_bf16 v[106:109], v[166:169], v[182:185], v[106:109]
	v_mfma_f32_16x16x32_bf16 v[98:101], v[158:161], v[190:193], v[98:101]
	v_mfma_f32_16x16x32_bf16 v[90:93], v[166:169], v[190:193], v[90:93]
	v_mfma_f32_16x16x32_bf16 v[82:85], v[158:161], v[202:205], v[82:85]
	v_mfma_f32_16x16x32_bf16 v[74:77], v[166:169], v[202:205], v[74:77]
	s_barrier
	s_add_i32 s75, s55, s40
	v_lshl_add_u64 v[146:147], s[30:31], 0, v[132:133]
	s_mov_b32 m0, s75
	ds_read_b128 v[206:209], v152
	ds_read_b128 v[210:213], v152 offset:1024
	ds_read_b128 v[214:217], v152 offset:2048
	ds_read_b128 v[218:221], v152 offset:3072
	global_load_lds_dwordx4 v[146:147], off
	v_lshl_add_u64 v[194:195], s[30:31], 0, v[136:137]
	s_add_i32 m0, s75, 0x2000
	s_nop 0
	global_load_lds_dwordx4 v[194:195], off
	s_barrier
	s_waitcnt lgkmcnt(0)
	s_waitcnt lgkmcnt(0)
	v_mfma_f32_16x16x32_bf16 v[118:121], v[206:209], v[170:173], v[118:121]
	v_mfma_f32_16x16x32_bf16 v[110:113], v[214:217], v[170:173], v[110:113]
	v_mfma_f32_16x16x32_bf16 v[102:105], v[206:209], v[178:181], v[102:105]
	v_mfma_f32_16x16x32_bf16 v[94:97], v[214:217], v[178:181], v[94:97]
	v_mfma_f32_16x16x32_bf16 v[86:89], v[206:209], v[186:189], v[86:89]
	v_mfma_f32_16x16x32_bf16 v[78:81], v[214:217], v[186:189], v[78:81]
	v_mfma_f32_16x16x32_bf16 v[70:73], v[206:209], v[198:201], v[70:73]
	v_mfma_f32_16x16x32_bf16 v[66:69], v[214:217], v[198:201], v[66:69]
	v_mfma_f32_16x16x32_bf16 v[118:121], v[210:213], v[174:177], v[118:121]
	v_mfma_f32_16x16x32_bf16 v[110:113], v[218:221], v[174:177], v[110:113]
	v_mfma_f32_16x16x32_bf16 v[102:105], v[210:213], v[182:185], v[102:105]
	v_mfma_f32_16x16x32_bf16 v[94:97], v[218:221], v[182:185], v[94:97]
	v_mfma_f32_16x16x32_bf16 v[86:89], v[210:213], v[190:193], v[86:89]
	v_mfma_f32_16x16x32_bf16 v[78:81], v[218:221], v[190:193], v[78:81]
	v_mfma_f32_16x16x32_bf16 v[70:73], v[210:213], v[202:205], v[70:73]
	v_mfma_f32_16x16x32_bf16 v[66:69], v[218:221], v[202:205], v[66:69]
	s_mov_b32 m0, s27
	v_lshl_add_u64 v[222:223], s[34:35], 0, v[130:131]
	s_barrier
	ds_read_b128 v[170:173], v151 offset:16384
	ds_read_b128 v[174:177], v151 offset:17408
	ds_read_b128 v[178:181], v151 offset:18432
	ds_read_b128 v[182:185], v151 offset:19456
	ds_read_b128 v[186:189], v151 offset:20480
	ds_read_b128 v[190:193], v151 offset:21504
	ds_read_b128 v[198:201], v151 offset:22528
	ds_read_b128 v[202:205], v151 offset:23552
	global_load_lds_dwordx4 v[222:223], off
	v_lshl_add_u64 v[224:225], s[34:35], 0, v[134:135]
	s_mov_b32 m0, s42
	s_nop 0
	global_load_lds_dwordx4 v[224:225], off
	s_waitcnt vmcnt(10)
	s_barrier
	s_waitcnt lgkmcnt(0)
	s_waitcnt lgkmcnt(0)
	v_mfma_f32_16x16x32_bf16 v[62:65], v[154:157], v[170:173], v[62:65]
	v_mfma_f32_16x16x32_bf16 v[58:61], v[162:165], v[170:173], v[58:61]
	v_mfma_f32_16x16x32_bf16 v[54:57], v[154:157], v[178:181], v[54:57]
	v_mfma_f32_16x16x32_bf16 v[46:49], v[162:165], v[178:181], v[46:49]
	v_mfma_f32_16x16x32_bf16 v[38:41], v[154:157], v[186:189], v[38:41]
	v_mfma_f32_16x16x32_bf16 v[30:33], v[162:165], v[186:189], v[30:33]
	v_mfma_f32_16x16x32_bf16 v[22:25], v[154:157], v[198:201], v[22:25]
	v_mfma_f32_16x16x32_bf16 v[14:17], v[162:165], v[198:201], v[14:17]
	v_mfma_f32_16x16x32_bf16 v[62:65], v[158:161], v[174:177], v[62:65]
	v_mfma_f32_16x16x32_bf16 v[58:61], v[166:169], v[174:177], v[58:61]
	v_mfma_f32_16x16x32_bf16 v[54:57], v[158:161], v[182:185], v[54:57]
	v_mfma_f32_16x16x32_bf16 v[46:49], v[166:169], v[182:185], v[46:49]
	v_mfma_f32_16x16x32_bf16 v[38:41], v[158:161], v[190:193], v[38:41]
	v_mfma_f32_16x16x32_bf16 v[30:33], v[166:169], v[190:193], v[30:33]
	v_mfma_f32_16x16x32_bf16 v[22:25], v[158:161], v[202:205], v[22:25]
	v_mfma_f32_16x16x32_bf16 v[14:17], v[166:169], v[202:205], v[14:17]
	s_barrier
	ds_read_b128 v[154:157], v150 offset:32768
	ds_read_b128 v[158:161], v150 offset:33792
	ds_read_b128 v[162:165], v150 offset:34816
	ds_read_b128 v[166:169], v150 offset:35840
	s_add_u32 s76, s30, 0x80000
	s_addc_u32 s77, s31, 0
	s_add_i32 s75, s64, s40
	v_lshl_add_u64 v[226:227], s[76:77], 0, v[132:133]
	s_mov_b32 m0, s75
	s_nop 0
	global_load_lds_dwordx4 v[226:227], off
	v_lshl_add_u64 v[226:227], s[76:77], 0, v[136:137]
	s_add_i32 m0, s75, 0x2000
	s_nop 0
	global_load_lds_dwordx4 v[226:227], off
	s_waitcnt vmcnt(6)
	s_barrier
	v_mfma_f32_16x16x32_bf16 v[50:53], v[206:209], v[170:173], v[50:53]
	v_mfma_f32_16x16x32_bf16 v[42:45], v[214:217], v[170:173], v[42:45]
	v_mfma_f32_16x16x32_bf16 v[34:37], v[206:209], v[178:181], v[34:37]
	v_mfma_f32_16x16x32_bf16 v[26:29], v[214:217], v[178:181], v[26:29]
	v_mfma_f32_16x16x32_bf16 v[18:21], v[206:209], v[186:189], v[18:21]
	v_mfma_f32_16x16x32_bf16 v[10:13], v[214:217], v[186:189], v[10:13]
	v_mfma_f32_16x16x32_bf16 v[6:9], v[206:209], v[198:201], v[6:9]
	v_mfma_f32_16x16x32_bf16 v[2:5], v[214:217], v[198:201], v[2:5]
	v_mfma_f32_16x16x32_bf16 v[50:53], v[210:213], v[174:177], v[50:53]
	v_mfma_f32_16x16x32_bf16 v[42:45], v[218:221], v[174:177], v[42:45]
	v_mfma_f32_16x16x32_bf16 v[34:37], v[210:213], v[182:185], v[34:37]
	v_mfma_f32_16x16x32_bf16 v[26:29], v[218:221], v[182:185], v[26:29]
	v_mfma_f32_16x16x32_bf16 v[18:21], v[210:213], v[190:193], v[18:21]
	v_mfma_f32_16x16x32_bf16 v[10:13], v[218:221], v[190:193], v[10:13]
	v_mfma_f32_16x16x32_bf16 v[6:9], v[210:213], v[202:205], v[6:9]
	v_mfma_f32_16x16x32_bf16 v[2:5], v[218:221], v[202:205], v[2:5]
	s_add_i32 s75, 0, 0x18000
	v_add_u32_e32 v153, s75, v148
	s_barrier
	s_add_u32 s34, s34, 0x80000
	s_addc_u32 s35, s35, 0
	s_mov_b32 m0, s43
	v_lshl_add_u64 v[206:207], s[34:35], 0, v[130:131]
	ds_read_b128 v[170:173], v151 offset:32768
	ds_read_b128 v[174:177], v151 offset:33792
	ds_read_b128 v[178:181], v151 offset:34816
	ds_read_b128 v[182:185], v151 offset:35840
	ds_read_b128 v[186:189], v151 offset:36864
	ds_read_b128 v[190:193], v151 offset:37888
	ds_read_b128 v[198:201], v151 offset:38912
	ds_read_b128 v[202:205], v151 offset:39936
	global_load_lds_dwordx4 v[206:207], off
	v_lshl_add_u64 v[206:207], s[34:35], 0, v[134:135]
	s_mov_b32 m0, s44
	s_nop 0
	global_load_lds_dwordx4 v[206:207], off
	s_waitcnt lgkmcnt(8)
	s_barrier
	s_waitcnt lgkmcnt(0)
	s_waitcnt lgkmcnt(0)
	v_mfma_f32_16x16x32_bf16 v[126:129], v[154:157], v[170:173], v[126:129]
	v_mfma_f32_16x16x32_bf16 v[122:125], v[162:165], v[170:173], v[122:125]
	v_mfma_f32_16x16x32_bf16 v[114:117], v[154:157], v[178:181], v[114:117]
	v_mfma_f32_16x16x32_bf16 v[106:109], v[162:165], v[178:181], v[106:109]
	v_mfma_f32_16x16x32_bf16 v[98:101], v[154:157], v[186:189], v[98:101]
	v_mfma_f32_16x16x32_bf16 v[90:93], v[162:165], v[186:189], v[90:93]
	v_mfma_f32_16x16x32_bf16 v[82:85], v[154:157], v[198:201], v[82:85]
	v_mfma_f32_16x16x32_bf16 v[74:77], v[162:165], v[198:201], v[74:77]
	v_mfma_f32_16x16x32_bf16 v[126:129], v[158:161], v[174:177], v[126:129]
	v_mfma_f32_16x16x32_bf16 v[122:125], v[166:169], v[174:177], v[122:125]
	v_mfma_f32_16x16x32_bf16 v[114:117], v[158:161], v[182:185], v[114:117]
	v_mfma_f32_16x16x32_bf16 v[106:109], v[166:169], v[182:185], v[106:109]
	v_mfma_f32_16x16x32_bf16 v[98:101], v[158:161], v[190:193], v[98:101]
	v_mfma_f32_16x16x32_bf16 v[90:93], v[166:169], v[190:193], v[90:93]
	v_mfma_f32_16x16x32_bf16 v[82:85], v[158:161], v[202:205], v[82:85]
	v_mfma_f32_16x16x32_bf16 v[74:77], v[166:169], v[202:205], v[74:77]
	s_barrier
	s_add_i32 s34, 0, 0x1c000
	s_add_i32 s35, s75, s40
	v_add_u32_e32 v153, s34, v148
	v_lshl_add_u64 v[146:147], v[146:147], 0, s[8:9]
	s_mov_b32 m0, s35
	ds_read_b128 v[206:209], v153
	ds_read_b128 v[210:213], v153 offset:1024
	ds_read_b128 v[214:217], v153 offset:2048
	ds_read_b128 v[218:221], v153 offset:3072
	global_load_lds_dwordx4 v[146:147], off
	v_lshl_add_u64 v[146:147], v[194:195], 0, s[8:9]
	s_add_i32 m0, s35, 0x2000
	s_nop 0
	global_load_lds_dwordx4 v[146:147], off
	s_barrier
	s_waitcnt lgkmcnt(0)
	s_waitcnt lgkmcnt(0)
	v_mfma_f32_16x16x32_bf16 v[118:121], v[206:209], v[170:173], v[118:121]
	v_mfma_f32_16x16x32_bf16 v[110:113], v[214:217], v[170:173], v[110:113]
	v_mfma_f32_16x16x32_bf16 v[102:105], v[206:209], v[178:181], v[102:105]
	v_mfma_f32_16x16x32_bf16 v[94:97], v[214:217], v[178:181], v[94:97]
	v_mfma_f32_16x16x32_bf16 v[86:89], v[206:209], v[186:189], v[86:89]
	v_mfma_f32_16x16x32_bf16 v[78:81], v[214:217], v[186:189], v[78:81]
	v_mfma_f32_16x16x32_bf16 v[70:73], v[206:209], v[198:201], v[70:73]
	v_mfma_f32_16x16x32_bf16 v[66:69], v[214:217], v[198:201], v[66:69]
	v_mfma_f32_16x16x32_bf16 v[118:121], v[210:213], v[174:177], v[118:121]
	v_mfma_f32_16x16x32_bf16 v[110:113], v[218:221], v[174:177], v[110:113]
	v_mfma_f32_16x16x32_bf16 v[102:105], v[210:213], v[182:185], v[102:105]
	v_mfma_f32_16x16x32_bf16 v[94:97], v[218:221], v[182:185], v[94:97]
	v_mfma_f32_16x16x32_bf16 v[86:89], v[210:213], v[190:193], v[86:89]
	v_mfma_f32_16x16x32_bf16 v[78:81], v[218:221], v[190:193], v[78:81]
	v_mfma_f32_16x16x32_bf16 v[70:73], v[210:213], v[202:205], v[70:73]
	v_mfma_f32_16x16x32_bf16 v[66:69], v[218:221], v[202:205], v[66:69]
	s_mov_b32 m0, s53
	v_lshl_add_u64 v[146:147], v[222:223], 0, s[8:9]
	s_barrier
	ds_read_b128 v[170:173], v151 offset:49152
	ds_read_b128 v[174:177], v151 offset:50176
	ds_read_b128 v[178:181], v151 offset:51200
	ds_read_b128 v[182:185], v151 offset:52224
	ds_read_b128 v[186:189], v151 offset:53248
	ds_read_b128 v[190:193], v151 offset:54272
	ds_read_b128 v[198:201], v151 offset:55296
	ds_read_b128 v[202:205], v151 offset:56320
	global_load_lds_dwordx4 v[146:147], off
	v_lshl_add_u64 v[146:147], v[224:225], 0, s[8:9]
	s_mov_b32 m0, s54
	s_nop 0
	global_load_lds_dwordx4 v[146:147], off
	s_waitcnt vmcnt(10)
	s_barrier
	s_waitcnt lgkmcnt(0)
	s_waitcnt lgkmcnt(0)
	v_mfma_f32_16x16x32_bf16 v[62:65], v[154:157], v[170:173], v[62:65]
	v_mfma_f32_16x16x32_bf16 v[58:61], v[162:165], v[170:173], v[58:61]
	v_mfma_f32_16x16x32_bf16 v[54:57], v[154:157], v[178:181], v[54:57]
	v_mfma_f32_16x16x32_bf16 v[46:49], v[162:165], v[178:181], v[46:49]
	v_mfma_f32_16x16x32_bf16 v[38:41], v[154:157], v[186:189], v[38:41]
	v_mfma_f32_16x16x32_bf16 v[30:33], v[162:165], v[186:189], v[30:33]
	v_mfma_f32_16x16x32_bf16 v[22:25], v[154:157], v[198:201], v[22:25]
	v_mfma_f32_16x16x32_bf16 v[14:17], v[162:165], v[198:201], v[14:17]
	v_mfma_f32_16x16x32_bf16 v[62:65], v[158:161], v[174:177], v[62:65]
	v_mfma_f32_16x16x32_bf16 v[58:61], v[166:169], v[174:177], v[58:61]
	v_mfma_f32_16x16x32_bf16 v[54:57], v[158:161], v[182:185], v[54:57]
	v_mfma_f32_16x16x32_bf16 v[46:49], v[166:169], v[182:185], v[46:49]
	v_mfma_f32_16x16x32_bf16 v[38:41], v[158:161], v[190:193], v[38:41]
	v_mfma_f32_16x16x32_bf16 v[30:33], v[166:169], v[190:193], v[30:33]
	v_mfma_f32_16x16x32_bf16 v[22:25], v[158:161], v[202:205], v[22:25]
	v_mfma_f32_16x16x32_bf16 v[14:17], v[166:169], v[202:205], v[14:17]
	s_barrier
	ds_read_b128 v[154:157], v150
	ds_read_b128 v[158:161], v150 offset:1024
	ds_read_b128 v[162:165], v150 offset:2048
	ds_read_b128 v[166:169], v150 offset:3072
	s_add_u32 s30, s30, 0x80080
	s_addc_u32 s31, s31, 0
	s_add_i32 s34, s34, s40
	v_lshl_add_u64 v[146:147], s[30:31], 0, v[132:133]
	s_mov_b32 m0, s34
	s_nop 0
	global_load_lds_dwordx4 v[146:147], off
	v_lshl_add_u64 v[146:147], s[30:31], 0, v[136:137]
	s_add_i32 m0, s34, 0x2000
	s_nop 0
	global_load_lds_dwordx4 v[146:147], off
	s_waitcnt vmcnt(6)
	s_barrier
	v_mfma_f32_16x16x32_bf16 v[50:53], v[206:209], v[170:173], v[50:53]
	v_mfma_f32_16x16x32_bf16 v[42:45], v[214:217], v[170:173], v[42:45]
	v_mfma_f32_16x16x32_bf16 v[34:37], v[206:209], v[178:181], v[34:37]
	v_mfma_f32_16x16x32_bf16 v[26:29], v[214:217], v[178:181], v[26:29]
	v_mfma_f32_16x16x32_bf16 v[18:21], v[206:209], v[186:189], v[18:21]
	v_mfma_f32_16x16x32_bf16 v[10:13], v[214:217], v[186:189], v[10:13]
	v_mfma_f32_16x16x32_bf16 v[6:9], v[206:209], v[198:201], v[6:9]
	v_mfma_f32_16x16x32_bf16 v[2:5], v[214:217], v[198:201], v[2:5]
	v_mfma_f32_16x16x32_bf16 v[50:53], v[210:213], v[174:177], v[50:53]
	v_mfma_f32_16x16x32_bf16 v[42:45], v[218:221], v[174:177], v[42:45]
	v_mfma_f32_16x16x32_bf16 v[34:37], v[210:213], v[182:185], v[34:37]
	v_mfma_f32_16x16x32_bf16 v[26:29], v[218:221], v[182:185], v[26:29]
	v_mfma_f32_16x16x32_bf16 v[18:21], v[210:213], v[190:193], v[18:21]
	v_mfma_f32_16x16x32_bf16 v[10:13], v[218:221], v[190:193], v[10:13]
	v_mfma_f32_16x16x32_bf16 v[6:9], v[210:213], v[202:205], v[6:9]
	v_mfma_f32_16x16x32_bf16 v[2:5], v[218:221], v[202:205], v[2:5]
	s_add_i32 s74, s74, 2
	s_add_u32 s28, s28, 0x100
	s_addc_u32 s29, s29, 0
	s_add_u32 s72, s72, 0x100
	s_addc_u32 s73, s73, 0
	s_cmp_gt_u32 s74, 29
	s_barrier
	s_cbranch_scc0 .LBB0_715
	s_waitcnt lgkmcnt(0)
	v_lshl_add_u32 v154, s26, 8, v1
	v_lshl_or_b32 v146, s69, 8, v149
	v_ashrrev_i32_e32 v155, 31, v154
	v_ashrrev_i32_e32 v147, 31, v146
	v_lshlrev_b64 v[156:157], 12, v[154:155]
	v_lshl_add_u64 v[156:157], s[6:7], 0, v[156:157]
	v_lshlrev_b64 v[158:159], 1, v[146:147]
	v_lshl_add_u64 v[146:147], v[156:157], 0, v[158:159]
	v_cvt_pk_bf16_f32 v126, v126, v127
	v_cvt_pk_bf16_f32 v127, v128, v129
	v_cvt_pk_bf16_f32 v128, v122, v123
	v_cvt_pk_bf16_f32 v129, v124, v125
	global_store_dwordx4 v[146:147], v[126:129], off
	v_cvt_pk_bf16_f32 v118, v118, v119
	v_cvt_pk_bf16_f32 v119, v120, v121
	v_cvt_pk_bf16_f32 v120, v110, v111
	v_or_b32_e32 v110, 16, v154
	v_ashrrev_i32_e32 v111, 31, v110
	v_lshlrev_b64 v[110:111], 12, v[110:111]
	v_lshl_add_u64 v[110:111], s[6:7], 0, v[110:111]
	v_cvt_pk_bf16_f32 v121, v112, v113
	global_store_dwordx4 v[146:147], v[118:121], off offset:256
	s_mov_b32 s69, s18
	s_mov_b32 s26, s20
	v_lshl_add_u64 v[118:119], v[110:111], 0, v[158:159]
	v_cvt_pk_bf16_f32 v110, v114, v115
	v_cvt_pk_bf16_f32 v111, v116, v117
	v_cvt_pk_bf16_f32 v112, v106, v107
	v_cvt_pk_bf16_f32 v113, v108, v109
	global_store_dwordx4 v[118:119], v[110:113], off
	v_cvt_pk_bf16_f32 v102, v102, v103
	v_cvt_pk_bf16_f32 v103, v104, v105
	v_cvt_pk_bf16_f32 v104, v94, v95
	v_or_b32_e32 v94, 32, v154
	v_ashrrev_i32_e32 v95, 31, v94
	v_lshlrev_b64 v[94:95], 12, v[94:95]
	v_lshl_add_u64 v[94:95], s[6:7], 0, v[94:95]
	v_cvt_pk_bf16_f32 v105, v96, v97
	global_store_dwordx4 v[118:119], v[102:105], off offset:256
	s_mov_b64 s[30:31], s[24:25]
	s_mov_b64 s[28:29], s[22:23]
	v_lshl_add_u64 v[102:103], v[94:95], 0, v[158:159]
	v_cvt_pk_bf16_f32 v94, v98, v99
	v_cvt_pk_bf16_f32 v95, v100, v101
	v_cvt_pk_bf16_f32 v96, v90, v91
	v_cvt_pk_bf16_f32 v97, v92, v93
	global_store_dwordx4 v[102:103], v[94:97], off
	v_cvt_pk_bf16_f32 v86, v86, v87
	v_cvt_pk_bf16_f32 v87, v88, v89
	v_cvt_pk_bf16_f32 v88, v78, v79
	v_or_b32_e32 v78, 48, v154
	v_ashrrev_i32_e32 v79, 31, v78
	v_lshlrev_b64 v[78:79], 12, v[78:79]
	v_lshl_add_u64 v[78:79], s[6:7], 0, v[78:79]
	v_cvt_pk_bf16_f32 v89, v80, v81
	global_store_dwordx4 v[102:103], v[86:89], off offset:256
	s_nop 1
	v_lshl_add_u64 v[86:87], v[78:79], 0, v[158:159]
	v_cvt_pk_bf16_f32 v78, v82, v83
	v_cvt_pk_bf16_f32 v79, v84, v85
	v_cvt_pk_bf16_f32 v80, v74, v75
	v_cvt_pk_bf16_f32 v81, v76, v77
	global_store_dwordx4 v[86:87], v[78:81], off
	v_cvt_pk_bf16_f32 v70, v70, v71
	v_cvt_pk_bf16_f32 v71, v72, v73
	v_cvt_pk_bf16_f32 v72, v66, v67
	v_cvt_pk_bf16_f32 v73, v68, v69
	global_store_dwordx4 v[86:87], v[70:73], off offset:256
	v_cvt_pk_bf16_f32 v62, v62, v63
	v_cvt_pk_bf16_f32 v63, v64, v65
	v_cvt_pk_bf16_f32 v64, v58, v59
	v_add_co_u32_e32 v58, vcc, s65, v146
	v_lshl_add_u64 v[66:67], v[146:147], 0, s[4:5]
	s_nop 0
	v_addc_co_u32_e32 v59, vcc, 0, v147, vcc
	v_cvt_pk_bf16_f32 v65, v60, v61
	global_store_dwordx4 v[58:59], v[62:65], off
	v_cvt_pk_bf16_f32 v50, v50, v51
	v_cvt_pk_bf16_f32 v51, v52, v53
	v_cvt_pk_bf16_f32 v52, v42, v43
	v_cvt_pk_bf16_f32 v53, v44, v45
	global_store_dwordx4 v[66:67], v[50:53], off offset:256
	v_cvt_pk_bf16_f32 v42, v54, v55
	v_cvt_pk_bf16_f32 v43, v56, v57
	v_cvt_pk_bf16_f32 v44, v46, v47
	v_add_co_u32_e32 v46, vcc, s66, v146
	s_nop 0
	v_lshl_add_u64 v[50:51], v[146:147], 0, s[10:11]
	v_addc_co_u32_e32 v47, vcc, 0, v147, vcc
	v_cvt_pk_bf16_f32 v45, v48, v49
	global_store_dwordx4 v[46:47], v[42:45], off
	v_cvt_pk_bf16_f32 v34, v34, v35
	v_cvt_pk_bf16_f32 v35, v36, v37
	v_cvt_pk_bf16_f32 v36, v26, v27
	v_cvt_pk_bf16_f32 v37, v28, v29
	global_store_dwordx4 v[50:51], v[34:37], off offset:256
	v_cvt_pk_bf16_f32 v26, v38, v39
	v_cvt_pk_bf16_f32 v27, v40, v41
	v_cvt_pk_bf16_f32 v28, v30, v31
	v_add_co_u32_e32 v30, vcc, s67, v146
	s_nop 0
	v_lshl_add_u64 v[34:35], v[146:147], 0, s[14:15]
	v_addc_co_u32_e32 v31, vcc, 0, v147, vcc
	v_cvt_pk_bf16_f32 v29, v32, v33
	global_store_dwordx4 v[30:31], v[26:29], off
	v_cvt_pk_bf16_f32 v18, v18, v19
	v_cvt_pk_bf16_f32 v19, v20, v21
	v_cvt_pk_bf16_f32 v20, v10, v11
	v_cvt_pk_bf16_f32 v21, v12, v13
	global_store_dwordx4 v[34:35], v[18:21], off offset:256
	v_cvt_pk_bf16_f32 v10, v22, v23
	v_cvt_pk_bf16_f32 v11, v24, v25
	v_cvt_pk_bf16_f32 v12, v14, v15
	v_add_co_u32_e32 v14, vcc, s68, v146
	s_nop 0
	v_lshl_add_u64 v[18:19], v[146:147], 0, s[16:17]
	v_addc_co_u32_e32 v15, vcc, 0, v147, vcc
	s_and_b64 vcc, exec, s[0:1]
	v_cvt_pk_bf16_f32 v13, v16, v17
	global_store_dwordx4 v[14:15], v[10:13], off
	v_cvt_pk_bf16_f32 v6, v6, v7
	v_cvt_pk_bf16_f32 v7, v8, v9
	v_cvt_pk_bf16_f32 v8, v2, v3
	v_cvt_pk_bf16_f32 v9, v4, v5
	global_store_dwordx4 v[18:19], v[6:9], off offset:256
	s_cbranch_vccz .LBB0_708
	s_waitcnt vmcnt(0)
	s_cmpk_gt_u32 s33, 0xff
	s_cbranch_scc1 .LBB0_719
	s_barrier

.LBB0_1059:
	s_ashr_i32 s21, s20, 31
	s_lshl_b64 s[6:7], s[20:21], 19
	s_add_u32 s6, s30, s6
	s_addc_u32 s7, s31, s7
	s_and_b64 s[4:5], s[4:5], exec
	s_cselect_b32 s21, s7, s25
	s_cselect_b32 s49, s6, s24
	v_mov_b32_e32 v181, v163
	v_mov_b32_e32 v183, v163
	s_add_u32 s50, s24, 0x100
	v_mov_b32_e32 v34, 0
	s_addc_u32 s51, s25, 0
	v_lshl_add_u64 v[184:185], s[14:15], 0, v[182:183]
	v_lshl_add_u64 v[186:187], s[14:15], 0, v[180:181]
	s_mov_b32 s52, -2
	s_mov_b64 s[26:27], 0
	v_mov_b32_e32 v35, v34
	v_mov_b32_e32 v36, v34
	v_mov_b32_e32 v37, v34
	v_mov_b32_e32 v42, v34
	v_mov_b32_e32 v43, v34
	v_mov_b32_e32 v44, v34
	v_mov_b32_e32 v45, v34
	v_mov_b32_e32 v50, v34
	v_mov_b32_e32 v51, v34
	v_mov_b32_e32 v52, v34
	v_mov_b32_e32 v53, v34
	v_mov_b32_e32 v58, v34
	v_mov_b32_e32 v59, v34
	v_mov_b32_e32 v60, v34
	v_mov_b32_e32 v61, v34
	v_mov_b32_e32 v66, v34
	v_mov_b32_e32 v67, v34
	v_mov_b32_e32 v68, v34
	v_mov_b32_e32 v69, v34
	v_mov_b32_e32 v74, v34
	v_mov_b32_e32 v75, v34
	v_mov_b32_e32 v76, v34
	v_mov_b32_e32 v77, v34
	v_mov_b32_e32 v82, v34
	v_mov_b32_e32 v83, v34
	v_mov_b32_e32 v84, v34
	v_mov_b32_e32 v85, v34
	v_mov_b32_e32 v90, v34
	v_mov_b32_e32 v91, v34
	v_mov_b32_e32 v92, v34
	v_mov_b32_e32 v93, v34
	v_mov_b32_e32 v38, v34
	v_mov_b32_e32 v39, v34
	v_mov_b32_e32 v40, v34
	v_mov_b32_e32 v41, v34
	v_mov_b32_e32 v46, v34
	v_mov_b32_e32 v47, v34
	v_mov_b32_e32 v48, v34
	v_mov_b32_e32 v49, v34
	v_mov_b32_e32 v54, v34
	v_mov_b32_e32 v55, v34
	v_mov_b32_e32 v56, v34
	v_mov_b32_e32 v57, v34
	v_mov_b32_e32 v62, v34
	v_mov_b32_e32 v63, v34
	v_mov_b32_e32 v64, v34
	v_mov_b32_e32 v65, v34
	v_mov_b32_e32 v70, v34
	v_mov_b32_e32 v71, v34
	v_mov_b32_e32 v72, v34
	v_mov_b32_e32 v73, v34
	v_mov_b32_e32 v78, v34
	v_mov_b32_e32 v79, v34
	v_mov_b32_e32 v80, v34
	v_mov_b32_e32 v81, v34
	v_mov_b32_e32 v86, v34
	v_mov_b32_e32 v87, v34
	v_mov_b32_e32 v88, v34
	v_mov_b32_e32 v89, v34
	v_mov_b32_e32 v94, v34
	v_mov_b32_e32 v95, v34
	v_mov_b32_e32 v96, v34
	v_mov_b32_e32 v97, v34
	v_mov_b32_e32 v98, v34
	v_mov_b32_e32 v99, v34
	v_mov_b32_e32 v100, v34
	v_mov_b32_e32 v101, v34
	v_mov_b32_e32 v106, v34
	v_mov_b32_e32 v107, v34
	v_mov_b32_e32 v108, v34
	v_mov_b32_e32 v109, v34
	v_mov_b32_e32 v114, v34
	v_mov_b32_e32 v115, v34
	v_mov_b32_e32 v116, v34
	v_mov_b32_e32 v117, v34
	v_mov_b32_e32 v122, v34
	v_mov_b32_e32 v123, v34
	v_mov_b32_e32 v124, v34
	v_mov_b32_e32 v125, v34
	v_mov_b32_e32 v130, v34
	v_mov_b32_e32 v131, v34
	v_mov_b32_e32 v132, v34
	v_mov_b32_e32 v133, v34
	v_mov_b32_e32 v138, v34
	v_mov_b32_e32 v139, v34
	v_mov_b32_e32 v140, v34
	v_mov_b32_e32 v141, v34
	v_mov_b32_e32 v146, v34
	v_mov_b32_e32 v147, v34
	v_mov_b32_e32 v148, v34
	v_mov_b32_e32 v149, v34
	v_mov_b32_e32 v154, v34
	v_mov_b32_e32 v155, v34
	v_mov_b32_e32 v156, v34
	v_mov_b32_e32 v157, v34
	v_mov_b32_e32 v102, v34
	v_mov_b32_e32 v103, v34
	v_mov_b32_e32 v104, v34
	v_mov_b32_e32 v105, v34
	v_mov_b32_e32 v110, v34
	v_mov_b32_e32 v111, v34
	v_mov_b32_e32 v112, v34
	v_mov_b32_e32 v113, v34
	v_mov_b32_e32 v118, v34
	v_mov_b32_e32 v119, v34
	v_mov_b32_e32 v120, v34
	v_mov_b32_e32 v121, v34
	v_mov_b32_e32 v126, v34
	v_mov_b32_e32 v127, v34
	v_mov_b32_e32 v128, v34
	v_mov_b32_e32 v129, v34
	v_mov_b32_e32 v134, v34
	v_mov_b32_e32 v135, v34
	v_mov_b32_e32 v136, v34
	v_mov_b32_e32 v137, v34
	v_mov_b32_e32 v142, v34
	v_mov_b32_e32 v143, v34
	v_mov_b32_e32 v144, v34
	v_mov_b32_e32 v145, v34
	v_mov_b32_e32 v150, v34
	v_mov_b32_e32 v151, v34
	v_mov_b32_e32 v152, v34
	v_mov_b32_e32 v153, v34
	v_mov_b32_e32 v158, v34
	v_mov_b32_e32 v159, v34
	v_mov_b32_e32 v160, v34
	v_mov_b32_e32 v161, v34
	v_add_u32_e32 v14, s39, v201
	ds_read_b128 v[2:5], v14
	ds_read_b128 v[6:9], v14 offset:1024
	ds_read_b128 v[10:13], v14 offset:2048
	ds_read_b128 v[14:17], v14 offset:3072
.LBB0_1060:
	s_add_u32 s4, s26, 0x100
	s_addc_u32 s5, s27, 0
	s_add_u32 s54, s50, s26
	s_addc_u32 s55, s51, s27
	s_cmp_eq_u32 s52, 12
	s_cselect_b64 vcc, -1, 0
	s_and_b64 s[24:25], vcc, exec
	s_cselect_b32 s53, 0, s4
	s_cselect_b32 s25, s21, s55
	s_cselect_b32 s24, s49, s54
	v_lshl_add_u64 v[18:19], v[186:187], 0, s[26:27]
	s_add_i32 m0, s33, 0xc000
	ds_read_b128 v[210:213], v203
	ds_read_b128 v[214:217], v203 offset:1024
	ds_read_b128 v[218:221], v203 offset:2048
	ds_read_b128 v[222:225], v203 offset:3072
	ds_read_b128 v[226:229], v203 offset:4096
	ds_read_b128 v[230:233], v203 offset:5120
	ds_read_b128 v[234:237], v203 offset:6144
	ds_read_b128 v[238:241], v203 offset:7168
	global_load_lds_dwordx4 v[18:19], off
	v_lshl_add_u64 v[18:19], v[184:185], 0, s[26:27]
	s_add_i32 m0, s33, 0xe000
	s_nop 0
	global_load_lds_dwordx4 v[18:19], off
	s_waitcnt lgkmcnt(8)
	s_barrier
	s_waitcnt lgkmcnt(0)
	s_waitcnt lgkmcnt(0)
	v_mfma_f32_16x16x128_f8f6f4 v[158:161], v[2:9], v[210:217], v[158:161]
	v_mfma_f32_16x16x128_f8f6f4 v[150:153], v[10:17], v[210:217], v[150:153]
	v_mfma_f32_16x16x128_f8f6f4 v[142:145], v[2:9], v[218:225], v[142:145]
	v_mfma_f32_16x16x128_f8f6f4 v[134:137], v[10:17], v[218:225], v[134:137]
	v_mfma_f32_16x16x128_f8f6f4 v[126:129], v[2:9], v[226:233], v[126:129]
	v_mfma_f32_16x16x128_f8f6f4 v[118:121], v[10:17], v[226:233], v[118:121]
	v_mfma_f32_16x16x128_f8f6f4 v[110:113], v[2:9], v[234:241], v[110:113]
	v_mfma_f32_16x16x128_f8f6f4 v[102:105], v[10:17], v[234:241], v[102:105]
	s_barrier
	s_add_i32 s26, s39, s23
	v_add_u32_e32 v30, s40, v201
	v_lshl_add_u64 v[188:189], s[24:25], 0, v[164:165]
	s_mov_b32 m0, s26
	ds_read_b128 v[18:21], v30
	ds_read_b128 v[22:25], v30 offset:1024
	ds_read_b128 v[26:29], v30 offset:2048
	ds_read_b128 v[30:33], v30 offset:3072
	global_load_lds_dwordx4 v[188:189], off
	v_lshl_add_u64 v[190:191], s[24:25], 0, v[166:167]
	s_add_i32 m0, s26, 0x2000
	s_nop 0
	global_load_lds_dwordx4 v[190:191], off
	s_barrier
	s_waitcnt lgkmcnt(0)
	s_waitcnt lgkmcnt(0)
	v_mfma_f32_16x16x128_f8f6f4 v[154:157], v[18:25], v[210:217], v[154:157]
	v_mfma_f32_16x16x128_f8f6f4 v[146:149], v[26:33], v[210:217], v[146:149]
	v_mfma_f32_16x16x128_f8f6f4 v[138:141], v[18:25], v[218:225], v[138:141]
	v_mfma_f32_16x16x128_f8f6f4 v[130:133], v[26:33], v[218:225], v[130:133]
	v_mfma_f32_16x16x128_f8f6f4 v[122:125], v[18:25], v[226:233], v[122:125]
	v_mfma_f32_16x16x128_f8f6f4 v[114:117], v[26:33], v[226:233], v[114:117]
	v_mfma_f32_16x16x128_f8f6f4 v[106:109], v[18:25], v[234:241], v[106:109]
	v_mfma_f32_16x16x128_f8f6f4 v[98:101], v[26:33], v[234:241], v[98:101]
	s_add_u32 s26, s10, s53
	s_mov_b32 m0, s33
	s_addc_u32 s27, s11, 0
	v_cndmask_b32_e32 v162, v208, v206, vcc
	s_barrier
	ds_read_b128 v[210:213], v203 offset:16384
	ds_read_b128 v[214:217], v203 offset:17408
	ds_read_b128 v[218:221], v203 offset:18432
	ds_read_b128 v[222:225], v203 offset:19456
	ds_read_b128 v[226:229], v203 offset:20480
	ds_read_b128 v[230:233], v203 offset:21504
	ds_read_b128 v[234:237], v203 offset:22528
	ds_read_b128 v[238:241], v203 offset:23552
	v_cndmask_b32_e32 v192, v178, v207, vcc
	global_load_lds_dwordx4 v162, s[26:27]
	s_mov_b32 m0, s34
	v_mov_b32_e32 v193, v163
	global_load_lds_dwordx4 v192, s[26:27]
	s_waitcnt vmcnt(10)
	s_barrier
	s_waitcnt lgkmcnt(0)
	v_lshl_add_u64 v[194:195], s[26:27], 0, v[162:163]
	v_lshl_add_u64 v[192:193], s[26:27], 0, v[192:193]
	s_waitcnt lgkmcnt(0)
	v_mfma_f32_16x16x128_f8f6f4 v[94:97], v[2:9], v[210:217], v[94:97]
	v_mfma_f32_16x16x128_f8f6f4 v[86:89], v[10:17], v[210:217], v[86:89]
	v_mfma_f32_16x16x128_f8f6f4 v[78:81], v[2:9], v[218:225], v[78:81]
	v_mfma_f32_16x16x128_f8f6f4 v[70:73], v[10:17], v[218:225], v[70:73]
	v_mfma_f32_16x16x128_f8f6f4 v[62:65], v[2:9], v[226:233], v[62:65]
	v_mfma_f32_16x16x128_f8f6f4 v[54:57], v[10:17], v[226:233], v[54:57]
	v_mfma_f32_16x16x128_f8f6f4 v[46:49], v[2:9], v[234:241], v[46:49]
	v_mfma_f32_16x16x128_f8f6f4 v[38:41], v[10:17], v[234:241], v[38:41]
	s_barrier
	v_add_u32_e32 v14, 0x18000, v201
	ds_read_b128 v[2:5], v14
	ds_read_b128 v[6:9], v14 offset:1024
	ds_read_b128 v[10:13], v14 offset:2048
	ds_read_b128 v[14:17], v14 offset:3072
	s_add_u32 s54, s24, 0x40000
	s_addc_u32 s55, s25, 0
	s_add_i32 s53, s40, s23
	v_lshl_add_u64 v[242:243], s[54:55], 0, v[164:165]
	s_mov_b32 m0, s53
	s_nop 0
	global_load_lds_dwordx4 v[242:243], off
	v_lshl_add_u64 v[242:243], s[54:55], 0, v[166:167]
	s_add_i32 m0, s53, 0x2000
	s_nop 0
	global_load_lds_dwordx4 v[242:243], off
	s_waitcnt vmcnt(6)
	s_barrier
	v_mfma_f32_16x16x128_f8f6f4 v[90:93], v[18:25], v[210:217], v[90:93]
	v_mfma_f32_16x16x128_f8f6f4 v[82:85], v[26:33], v[210:217], v[82:85]
	v_mfma_f32_16x16x128_f8f6f4 v[74:77], v[18:25], v[218:225], v[74:77]
	v_mfma_f32_16x16x128_f8f6f4 v[66:69], v[26:33], v[218:225], v[66:69]
	v_mfma_f32_16x16x128_f8f6f4 v[58:61], v[18:25], v[226:233], v[58:61]
	v_mfma_f32_16x16x128_f8f6f4 v[50:53], v[26:33], v[226:233], v[50:53]
	v_mfma_f32_16x16x128_f8f6f4 v[42:45], v[18:25], v[234:241], v[42:45]
	v_mfma_f32_16x16x128_f8f6f4 v[34:37], v[26:33], v[234:241], v[34:37]
	s_add_i32 s53, 0, 0x18000
	s_barrier
	v_cndmask_b32_e32 v172, v180, v174, vcc
	s_mov_b32 m0, s35
	v_cndmask_b32_e32 v226, v182, v176, vcc
	v_mov_b32_e32 v227, v173
	v_lshl_add_u64 v[228:229], s[26:27], 0, v[172:173]
	ds_read_b128 v[18:21], v203 offset:32768
	ds_read_b128 v[22:25], v203 offset:33792
	ds_read_b128 v[26:29], v203 offset:34816
	ds_read_b128 v[30:33], v203 offset:35840
	ds_read_b128 v[210:213], v203 offset:36864
	ds_read_b128 v[214:217], v203 offset:37888
	ds_read_b128 v[218:221], v203 offset:38912
	ds_read_b128 v[222:225], v203 offset:39936
	global_load_lds_dwordx4 v[228:229], off
	v_lshl_add_u64 v[226:227], s[26:27], 0, v[226:227]
	s_mov_b32 m0, s36
	s_nop 0
	global_load_lds_dwordx4 v[226:227], off
	s_waitcnt lgkmcnt(8)
	s_barrier
	s_waitcnt lgkmcnt(0)
	s_waitcnt lgkmcnt(0)
	v_mfma_f32_16x16x128_f8f6f4 v[158:161], v[2:9], v[18:25], v[158:161]
	v_mfma_f32_16x16x128_f8f6f4 v[150:153], v[10:17], v[18:25], v[150:153]
	v_mfma_f32_16x16x128_f8f6f4 v[142:145], v[2:9], v[26:33], v[142:145]
	v_mfma_f32_16x16x128_f8f6f4 v[134:137], v[10:17], v[26:33], v[134:137]
	v_mfma_f32_16x16x128_f8f6f4 v[126:129], v[2:9], v[210:217], v[126:129]
	v_mfma_f32_16x16x128_f8f6f4 v[118:121], v[10:17], v[210:217], v[118:121]
	v_mfma_f32_16x16x128_f8f6f4 v[110:113], v[2:9], v[218:225], v[110:113]
	v_mfma_f32_16x16x128_f8f6f4 v[102:105], v[10:17], v[218:225], v[102:105]
	s_barrier
	s_add_i32 s26, 0, 0x1c000
	s_add_i32 s27, s53, s23
	v_add_u32_e32 v162, s26, v201
	v_lshl_add_u64 v[188:189], v[188:189], 0, s[16:17]
	s_mov_b32 m0, s27
	ds_read_b128 v[226:229], v162
	ds_read_b128 v[230:233], v162 offset:1024
	ds_read_b128 v[234:237], v162 offset:2048
	ds_read_b128 v[238:241], v162 offset:3072
	global_load_lds_dwordx4 v[188:189], off
	v_lshl_add_u64 v[188:189], v[190:191], 0, s[16:17]
	s_add_i32 m0, s27, 0x2000
	s_nop 0
	global_load_lds_dwordx4 v[188:189], off
	s_barrier
	s_waitcnt lgkmcnt(0)
	s_waitcnt lgkmcnt(0)
	v_mfma_f32_16x16x128_f8f6f4 v[154:157], v[226:233], v[18:25], v[154:157]
	v_mfma_f32_16x16x128_f8f6f4 v[146:149], v[234:241], v[18:25], v[146:149]
	v_mfma_f32_16x16x128_f8f6f4 v[138:141], v[226:233], v[26:33], v[138:141]
	v_mfma_f32_16x16x128_f8f6f4 v[130:133], v[234:241], v[26:33], v[130:133]
	v_mfma_f32_16x16x128_f8f6f4 v[122:125], v[226:233], v[210:217], v[122:125]
	v_mfma_f32_16x16x128_f8f6f4 v[114:117], v[234:241], v[210:217], v[114:117]
	v_mfma_f32_16x16x128_f8f6f4 v[106:109], v[226:233], v[218:225], v[106:109]
	v_mfma_f32_16x16x128_f8f6f4 v[98:101], v[234:241], v[218:225], v[98:101]
	s_mov_b32 m0, s37
	v_lshl_add_u64 v[188:189], v[194:195], 0, s[16:17]
	s_barrier
	ds_read_b128 v[18:21], v203 offset:49152
	ds_read_b128 v[22:25], v203 offset:50176
	ds_read_b128 v[26:29], v203 offset:51200
	ds_read_b128 v[30:33], v203 offset:52224
	ds_read_b128 v[210:213], v203 offset:53248
	ds_read_b128 v[214:217], v203 offset:54272
	ds_read_b128 v[218:221], v203 offset:55296
	ds_read_b128 v[222:225], v203 offset:56320
	global_load_lds_dwordx4 v[188:189], off
	v_lshl_add_u64 v[188:189], v[192:193], 0, s[16:17]
	s_mov_b32 m0, s38
	s_nop 0
	global_load_lds_dwordx4 v[188:189], off
	s_waitcnt vmcnt(10)
	s_barrier
	s_waitcnt lgkmcnt(0)
	s_waitcnt lgkmcnt(0)
	v_mfma_f32_16x16x128_f8f6f4 v[94:97], v[2:9], v[18:25], v[94:97]
	v_mfma_f32_16x16x128_f8f6f4 v[86:89], v[10:17], v[18:25], v[86:89]
	v_mfma_f32_16x16x128_f8f6f4 v[78:81], v[2:9], v[26:33], v[78:81]
	v_mfma_f32_16x16x128_f8f6f4 v[70:73], v[10:17], v[26:33], v[70:73]
	v_mfma_f32_16x16x128_f8f6f4 v[62:65], v[2:9], v[210:217], v[62:65]
	v_mfma_f32_16x16x128_f8f6f4 v[54:57], v[10:17], v[210:217], v[54:57]
	v_mfma_f32_16x16x128_f8f6f4 v[46:49], v[2:9], v[218:225], v[46:49]
	v_mfma_f32_16x16x128_f8f6f4 v[38:41], v[10:17], v[218:225], v[38:41]
	s_barrier
	v_add_u32_e32 v14, s39, v201
	ds_read_b128 v[2:5], v14
	ds_read_b128 v[6:9], v14 offset:1024
	ds_read_b128 v[10:13], v14 offset:2048
	ds_read_b128 v[14:17], v14 offset:3072
	s_add_u32 s24, s24, 0x40080
	s_addc_u32 s25, s25, 0
	s_add_i32 s26, s26, s23
	v_lshl_add_u64 v[242:243], s[24:25], 0, v[164:165]
	s_mov_b32 m0, s26
	s_nop 0
	global_load_lds_dwordx4 v[242:243], off
	v_lshl_add_u64 v[242:243], s[24:25], 0, v[166:167]
	s_add_i32 m0, s26, 0x2000
	s_nop 0
	global_load_lds_dwordx4 v[242:243], off
	s_waitcnt vmcnt(6)
	s_barrier
	v_mfma_f32_16x16x128_f8f6f4 v[90:93], v[226:233], v[18:25], v[90:93]
	v_mfma_f32_16x16x128_f8f6f4 v[82:85], v[234:241], v[18:25], v[82:85]
	v_mfma_f32_16x16x128_f8f6f4 v[74:77], v[226:233], v[26:33], v[74:77]
	v_mfma_f32_16x16x128_f8f6f4 v[66:69], v[234:241], v[26:33], v[66:69]
	v_mfma_f32_16x16x128_f8f6f4 v[58:61], v[226:233], v[210:217], v[58:61]
	v_mfma_f32_16x16x128_f8f6f4 v[50:53], v[234:241], v[210:217], v[50:53]
	v_mfma_f32_16x16x128_f8f6f4 v[42:45], v[226:233], v[218:225], v[42:45]
	v_mfma_f32_16x16x128_f8f6f4 v[34:37], v[234:241], v[218:225], v[34:37]
	s_add_i32 s52, s52, 2
	s_cmp_gt_u32 s52, 13
	s_mov_b64 s[26:27], s[4:5]
	s_barrier
	s_cbranch_scc0 .LBB0_1060
	s_waitcnt lgkmcnt(0)
	v_mov_b32_e32 v2, v158
	v_mov_b32_e32 v3, v154
	v_pk_mul_f32 v[2:3], v[2:3], s[18:19] op_sel_hi:[1,0]
	v_mov_b32_e32 v154, v159
	v_mul_f32_e32 v5, 0xbfb8aa3b, v2
	v_pk_mul_f32 v[6:7], v[154:155], s[18:19] op_sel_hi:[1,0]
	v_exp_f32_e32 v8, v5
	v_mul_f32_e32 v5, 0xbfb8aa3b, v6
	v_exp_f32_e32 v9, v5
	v_mul_f32_e32 v2, v2, v3
	v_add_f32_e32 v8, 1.0, v8
	v_rcp_f32_e32 v8, v8
	v_add_f32_e32 v9, 1.0, v9
	v_rcp_f32_e32 v9, v9
	v_mov_b32_e32 v3, v156
	v_mul_f32_e32 v8, v8, v2
	v_mul_f32_e32 v2, v6, v7
	v_mul_f32_e32 v9, v9, v2
	v_mov_b32_e32 v2, v160
	v_pk_mul_f32 v[2:3], v[2:3], s[18:19] op_sel_hi:[1,0]
	v_mov_b32_e32 v156, v161
	v_mul_f32_e32 v6, 0xbfb8aa3b, v2
	v_exp_f32_e32 v10, v6
	v_pk_mul_f32 v[6:7], v[156:157], s[18:19] op_sel_hi:[1,0]
	v_mul_f32_e32 v12, v2, v3
	v_mul_f32_e32 v11, 0xbfb8aa3b, v6
	v_exp_f32_e32 v11, v11
	v_add_f32_e32 v2, 1.0, v10
	v_rcp_f32_e32 v10, v2
	v_mov_b32_e32 v3, v146
	v_add_f32_e32 v2, 1.0, v11
	v_rcp_f32_e32 v11, v2
	v_mov_b32_e32 v2, v150
	v_pk_mul_f32 v[2:3], v[2:3], s[18:19] op_sel_hi:[1,0]
	v_mul_f32_e32 v6, v6, v7
	v_mul_f32_e32 v13, 0xbfb8aa3b, v2
	v_exp_f32_e32 v13, v13
	v_mul_f32_e32 v11, v11, v6
	v_mov_b32_e32 v146, v151
	v_mul_f32_e32 v10, v10, v12
	v_add_f32_e32 v6, 1.0, v13
	v_rcp_f32_e32 v12, v6
	v_pk_mul_f32 v[6:7], v[146:147], s[18:19] op_sel_hi:[1,0]
	v_mul_f32_e32 v2, v2, v3
	v_mul_f32_e32 v13, 0xbfb8aa3b, v6
	v_exp_f32_e32 v13, v13
	v_mul_f32_e32 v12, v12, v2
	v_mov_b32_e32 v3, v148
	v_mul_f32_e32 v14, v6, v7
	v_add_f32_e32 v2, 1.0, v13
	v_rcp_f32_e32 v13, v2
	v_mov_b32_e32 v2, v152
	v_pk_mul_f32 v[2:3], v[2:3], s[18:19] op_sel_hi:[1,0]
	v_mov_b32_e32 v148, v153
	v_mul_f32_e32 v6, 0xbfb8aa3b, v2
	v_exp_f32_e32 v15, v6
	v_pk_mul_f32 v[6:7], v[148:149], s[18:19] op_sel_hi:[1,0]
	v_mul_f32_e32 v13, v13, v14
	v_mul_f32_e32 v16, 0xbfb8aa3b, v6
	v_exp_f32_e32 v16, v16
	v_add_f32_e32 v14, 1.0, v15
	v_rcp_f32_e32 v14, v14
	v_mul_f32_e32 v2, v2, v3
	v_add_f32_e32 v15, 1.0, v16
	v_rcp_f32_e32 v15, v15
	v_mul_f32_e32 v3, v6, v7
	v_mul_f32_e32 v6, 4.0, v8
	v_mul_f32_e32 v7, 4.0, v9
	v_mul_f32_e32 v8, 4.0, v10
	v_mul_f32_e32 v9, 4.0, v11
	v_mul_f32_e32 v10, 4.0, v12
	v_mul_f32_e32 v11, 4.0, v13
	v_med3_f32 v12, v6, s41, v205
	v_med3_f32 v7, v7, s41, v205
	v_mov_b32_e32 v6, v163
	v_cvt_pk_fp8_f32 v6, v12, v7
	v_med3_f32 v10, v10, s41, v205
	v_med3_f32 v11, v11, s41, v205
	v_mov_b32_e32 v7, v163
	v_cvt_pk_fp8_f32 v7, v10, v11
	v_mul_f32_e32 v2, v14, v2
	v_mul_f32_e32 v3, v15, v3
	v_mul_f32_e32 v2, 4.0, v2
	v_mul_f32_e32 v3, 4.0, v3
	v_lshl_add_u32 v4, s48, 8, v179
	v_med3_f32 v8, v8, s41, v205
	v_med3_f32 v9, v9, s41, v205
	v_med3_f32 v2, v2, s41, v205
	v_med3_f32 v3, v3, s41, v205
	s_lshl_b32 s4, s22, 7
	v_ashrrev_i32_e32 v5, 31, v4
	v_cvt_pk_fp8_f32 v6, v8, v9 op_sel:[0,0,1]
	v_cvt_pk_fp8_f32 v7, v2, v3 op_sel:[0,0,1]
	s_and_b32 s4, s4, 0x780
	v_lshlrev_b64 v[2:3], 11, v[4:5]
	v_mov_b32_e32 v8, v142
	v_mov_b32_e32 v9, v138
	v_or_b32_e32 v162, s4, v202
	v_lshl_add_u64 v[2:3], s[12:13], 0, v[2:3]
	v_pk_mul_f32 v[8:9], v[8:9], s[18:19] op_sel_hi:[1,0]
	v_mov_b32_e32 v138, v143
	v_lshl_add_u64 v[2:3], v[2:3], 0, v[162:163]
	v_mul_f32_e32 v5, 0xbfb8aa3b, v8
	v_pk_mul_f32 v[10:11], v[138:139], s[18:19] op_sel_hi:[1,0]
	s_nop 15
	s_nop 15
	global_store_dwordx2 v[2:3], v[6:7], off
	v_exp_f32_e32 v5, v5
	v_mul_f32_e32 v7, 0xbfb8aa3b, v10
	v_exp_f32_e32 v12, v7
	v_mul_f32_e32 v8, v8, v9
	v_add_f32_e32 v5, 1.0, v5
	v_rcp_f32_e32 v5, v5
	v_add_f32_e32 v12, 1.0, v12
	v_rcp_f32_e32 v12, v12
	v_mov_b32_e32 v9, v140
	v_mul_f32_e32 v5, v5, v8
	v_mul_f32_e32 v8, v10, v11
	v_mul_f32_e32 v12, v12, v8
	v_mov_b32_e32 v8, v144
	v_pk_mul_f32 v[8:9], v[8:9], s[18:19] op_sel_hi:[1,0]
	v_mov_b32_e32 v140, v145
	v_mul_f32_e32 v10, 0xbfb8aa3b, v8
	v_exp_f32_e32 v13, v10
	v_pk_mul_f32 v[10:11], v[140:141], s[18:19] op_sel_hi:[1,0]
	v_mul_f32_e32 v15, v8, v9
	v_mul_f32_e32 v14, 0xbfb8aa3b, v10
	v_exp_f32_e32 v14, v14
	v_add_f32_e32 v8, 1.0, v13
	v_rcp_f32_e32 v13, v8
	v_mov_b32_e32 v9, v130
	v_add_f32_e32 v8, 1.0, v14
	v_rcp_f32_e32 v14, v8
	v_mov_b32_e32 v8, v134
	v_pk_mul_f32 v[8:9], v[8:9], s[18:19] op_sel_hi:[1,0]
	v_mul_f32_e32 v10, v10, v11
	v_mul_f32_e32 v16, 0xbfb8aa3b, v8
	v_exp_f32_e32 v16, v16
	v_mul_f32_e32 v14, v14, v10
	v_mov_b32_e32 v130, v135
	v_mul_f32_e32 v13, v13, v15
	v_add_f32_e32 v10, 1.0, v16
	v_rcp_f32_e32 v15, v10
	v_pk_mul_f32 v[10:11], v[130:131], s[18:19] op_sel_hi:[1,0]
	v_mul_f32_e32 v8, v8, v9
	v_mul_f32_e32 v16, 0xbfb8aa3b, v10
	v_exp_f32_e32 v16, v16
	v_mul_f32_e32 v15, v15, v8
	v_mov_b32_e32 v9, v132
	v_mul_f32_e32 v17, v10, v11
	v_add_f32_e32 v8, 1.0, v16
	v_rcp_f32_e32 v16, v8
	v_mov_b32_e32 v8, v136
	v_pk_mul_f32 v[8:9], v[8:9], s[18:19] op_sel_hi:[1,0]
	v_mov_b32_e32 v132, v137
	v_mul_f32_e32 v10, 0xbfb8aa3b, v8
	v_exp_f32_e32 v18, v10
	v_pk_mul_f32 v[10:11], v[132:133], s[18:19] op_sel_hi:[1,0]
	v_mul_f32_e32 v16, v16, v17
	v_mul_f32_e32 v19, 0xbfb8aa3b, v10
	v_exp_f32_e32 v19, v19
	v_add_f32_e32 v17, 1.0, v18
	v_rcp_f32_e32 v17, v17
	v_mul_f32_e32 v8, v8, v9
	v_add_f32_e32 v18, 1.0, v19
	v_rcp_f32_e32 v18, v18
	v_mul_f32_e32 v9, v10, v11
	v_mul_f32_e32 v8, v17, v8
	v_mul_f32_e32 v5, 4.0, v5
	v_mul_f32_e32 v9, v18, v9
	v_mul_f32_e32 v10, 4.0, v12
	v_mul_f32_e32 v11, 4.0, v13
	v_mul_f32_e32 v12, 4.0, v14
	v_mul_f32_e32 v13, 4.0, v15
	v_mul_f32_e32 v14, 4.0, v16
	v_mul_f32_e32 v15, 4.0, v8
	v_mul_f32_e32 v16, 4.0, v9
	v_med3_f32 v5, v5, s41, v205
	v_med3_f32 v9, v10, s41, v205
	v_mov_b32_e32 v8, v163
	v_cvt_pk_fp8_f32 v8, v5, v9
	v_med3_f32 v5, v11, s41, v205
	v_med3_f32 v10, v12, s41, v205
	v_med3_f32 v11, v13, s41, v205
	v_med3_f32 v12, v14, s41, v205
	v_mov_b32_e32 v9, v163
	v_cvt_pk_fp8_f32 v9, v11, v12
	v_or_b32_e32 v6, 16, v4
	v_cvt_pk_fp8_f32 v8, v5, v10 op_sel:[0,0,1]
	v_med3_f32 v5, v15, s41, v205
	v_med3_f32 v10, v16, s41, v205
	v_ashrrev_i32_e32 v7, 31, v6
	v_cvt_pk_fp8_f32 v9, v5, v10 op_sel:[0,0,1]
	v_lshlrev_b64 v[6:7], 11, v[6:7]
	v_lshl_add_u64 v[6:7], s[12:13], 0, v[6:7]
	v_lshl_add_u64 v[6:7], v[6:7], 0, v[162:163]
	global_store_dwordx2 v[6:7], v[8:9], off
	v_mov_b32_e32 v8, v126
	v_mov_b32_e32 v9, v122
	v_pk_mul_f32 v[8:9], v[8:9], s[18:19] op_sel_hi:[1,0]
	v_mov_b32_e32 v122, v127
	v_mul_f32_e32 v5, 0xbfb8aa3b, v8
	v_pk_mul_f32 v[10:11], v[122:123], s[18:19] op_sel_hi:[1,0]
	v_exp_f32_e32 v5, v5
	v_mul_f32_e32 v7, 0xbfb8aa3b, v10
	v_exp_f32_e32 v12, v7
	v_mul_f32_e32 v8, v8, v9
	v_add_f32_e32 v5, 1.0, v5
	v_rcp_f32_e32 v5, v5
	v_add_f32_e32 v12, 1.0, v12
	v_rcp_f32_e32 v12, v12
	v_mov_b32_e32 v9, v124
	v_mul_f32_e32 v5, v5, v8
	v_mul_f32_e32 v8, v10, v11
	v_mul_f32_e32 v12, v12, v8
	v_mov_b32_e32 v8, v128
	v_pk_mul_f32 v[8:9], v[8:9], s[18:19] op_sel_hi:[1,0]
	v_mov_b32_e32 v124, v129
	v_mul_f32_e32 v10, 0xbfb8aa3b, v8
	v_exp_f32_e32 v13, v10
	v_pk_mul_f32 v[10:11], v[124:125], s[18:19] op_sel_hi:[1,0]
	v_mul_f32_e32 v15, v8, v9
	v_mul_f32_e32 v14, 0xbfb8aa3b, v10
	v_exp_f32_e32 v14, v14
	v_add_f32_e32 v8, 1.0, v13
	v_rcp_f32_e32 v13, v8
	v_mov_b32_e32 v9, v114
	v_add_f32_e32 v8, 1.0, v14
	v_rcp_f32_e32 v14, v8
	v_mov_b32_e32 v8, v118
	v_pk_mul_f32 v[8:9], v[8:9], s[18:19] op_sel_hi:[1,0]
	v_mul_f32_e32 v10, v10, v11
	v_mul_f32_e32 v16, 0xbfb8aa3b, v8
	v_exp_f32_e32 v16, v16
	v_mul_f32_e32 v14, v14, v10
	v_mov_b32_e32 v114, v119
	v_mul_f32_e32 v13, v13, v15
	v_add_f32_e32 v10, 1.0, v16
	v_rcp_f32_e32 v15, v10
	v_pk_mul_f32 v[10:11], v[114:115], s[18:19] op_sel_hi:[1,0]
	v_mul_f32_e32 v8, v8, v9
	v_mul_f32_e32 v16, 0xbfb8aa3b, v10
	v_exp_f32_e32 v16, v16
	v_mul_f32_e32 v15, v15, v8
	v_mov_b32_e32 v9, v116
	v_mul_f32_e32 v17, v10, v11
	v_add_f32_e32 v8, 1.0, v16
	v_rcp_f32_e32 v16, v8
	v_mov_b32_e32 v8, v120
	v_pk_mul_f32 v[8:9], v[8:9], s[18:19] op_sel_hi:[1,0]
	v_mov_b32_e32 v116, v121
	v_mul_f32_e32 v10, 0xbfb8aa3b, v8
	v_exp_f32_e32 v18, v10
	v_pk_mul_f32 v[10:11], v[116:117], s[18:19] op_sel_hi:[1,0]
	v_mul_f32_e32 v16, v16, v17
	v_mul_f32_e32 v19, 0xbfb8aa3b, v10
	v_exp_f32_e32 v19, v19
	v_add_f32_e32 v17, 1.0, v18
	v_rcp_f32_e32 v17, v17
	v_mul_f32_e32 v8, v8, v9
	v_add_f32_e32 v18, 1.0, v19
	v_rcp_f32_e32 v18, v18
	v_mul_f32_e32 v9, v10, v11
	v_mul_f32_e32 v8, v17, v8
	v_mul_f32_e32 v5, 4.0, v5
	v_mul_f32_e32 v9, v18, v9
	v_mul_f32_e32 v10, 4.0, v12
	v_mul_f32_e32 v11, 4.0, v13
	v_mul_f32_e32 v12, 4.0, v14
	v_mul_f32_e32 v13, 4.0, v15
	v_mul_f32_e32 v14, 4.0, v16
	v_mul_f32_e32 v15, 4.0, v8
	v_mul_f32_e32 v16, 4.0, v9
	v_med3_f32 v5, v5, s41, v205
	v_med3_f32 v9, v10, s41, v205
	v_mov_b32_e32 v8, v163
	v_cvt_pk_fp8_f32 v8, v5, v9
	v_med3_f32 v5, v11, s41, v205
	v_med3_f32 v10, v12, s41, v205
	v_med3_f32 v11, v13, s41, v205
	v_med3_f32 v12, v14, s41, v205
	v_mov_b32_e32 v9, v163
	v_cvt_pk_fp8_f32 v9, v11, v12
	v_or_b32_e32 v6, 32, v4
	v_cvt_pk_fp8_f32 v8, v5, v10 op_sel:[0,0,1]
	v_med3_f32 v5, v15, s41, v205
	v_med3_f32 v10, v16, s41, v205
	v_ashrrev_i32_e32 v7, 31, v6
	v_cvt_pk_fp8_f32 v9, v5, v10 op_sel:[0,0,1]
	v_lshlrev_b64 v[6:7], 11, v[6:7]
	v_lshl_add_u64 v[6:7], s[12:13], 0, v[6:7]
	v_lshl_add_u64 v[6:7], v[6:7], 0, v[162:163]
	global_store_dwordx2 v[6:7], v[8:9], off
	v_mov_b32_e32 v6, v110
	v_mov_b32_e32 v7, v106
	v_pk_mul_f32 v[6:7], v[6:7], s[18:19] op_sel_hi:[1,0]
	v_mov_b32_e32 v106, v111
	v_mul_f32_e32 v8, 0xbfb8aa3b, v6
	v_exp_f32_e32 v10, v8
	v_pk_mul_f32 v[8:9], v[106:107], s[18:19] op_sel_hi:[1,0]
	v_mul_f32_e32 v6, v6, v7
	v_mul_f32_e32 v11, 0xbfb8aa3b, v8
	v_exp_f32_e32 v11, v11
	v_add_f32_e32 v10, 1.0, v10
	v_rcp_f32_e32 v10, v10
	v_mov_b32_e32 v7, v108
	v_add_f32_e32 v11, 1.0, v11
	v_rcp_f32_e32 v11, v11
	v_mul_f32_e32 v10, v10, v6
	v_mul_f32_e32 v6, v8, v9
	v_mov_b32_e32 v108, v113
	v_mul_f32_e32 v11, v11, v6
	v_mov_b32_e32 v6, v112
	v_pk_mul_f32 v[6:7], v[6:7], s[18:19] op_sel_hi:[1,0]
	v_or_b32_e32 v4, 48, v4
	v_mul_f32_e32 v8, 0xbfb8aa3b, v6
	v_exp_f32_e32 v12, v8
	v_pk_mul_f32 v[8:9], v[108:109], s[18:19] op_sel_hi:[1,0]
	v_mul_f32_e32 v14, v6, v7
	v_mul_f32_e32 v13, 0xbfb8aa3b, v8
	v_exp_f32_e32 v13, v13
	v_add_f32_e32 v6, 1.0, v12
	v_rcp_f32_e32 v12, v6
	v_mov_b32_e32 v7, v98
	v_add_f32_e32 v6, 1.0, v13
	v_rcp_f32_e32 v13, v6
	v_mov_b32_e32 v6, v102
	v_pk_mul_f32 v[6:7], v[6:7], s[18:19] op_sel_hi:[1,0]
	v_mul_f32_e32 v8, v8, v9
	v_mul_f32_e32 v15, 0xbfb8aa3b, v6
	v_exp_f32_e32 v15, v15
	v_mul_f32_e32 v13, v13, v8
	v_mov_b32_e32 v98, v103
	v_mul_f32_e32 v12, v12, v14
	v_add_f32_e32 v8, 1.0, v15
	v_rcp_f32_e32 v14, v8
	v_pk_mul_f32 v[8:9], v[98:99], s[18:19] op_sel_hi:[1,0]
	v_mul_f32_e32 v6, v6, v7
	v_mul_f32_e32 v15, 0xbfb8aa3b, v8
	v_exp_f32_e32 v15, v15
	v_mul_f32_e32 v14, v14, v6
	v_mov_b32_e32 v7, v100
	v_mul_f32_e32 v16, v8, v9
	v_add_f32_e32 v6, 1.0, v15
	v_rcp_f32_e32 v15, v6
	v_mov_b32_e32 v6, v104
	v_pk_mul_f32 v[6:7], v[6:7], s[18:19] op_sel_hi:[1,0]
	v_mov_b32_e32 v100, v105
	v_mul_f32_e32 v8, 0xbfb8aa3b, v6
	v_exp_f32_e32 v17, v8
	v_pk_mul_f32 v[8:9], v[100:101], s[18:19] op_sel_hi:[1,0]
	v_mul_f32_e32 v15, v15, v16
	v_mul_f32_e32 v18, 0xbfb8aa3b, v8
	v_exp_f32_e32 v18, v18
	v_add_f32_e32 v16, 1.0, v17
	v_rcp_f32_e32 v16, v16
	v_mul_f32_e32 v6, v6, v7
	v_add_f32_e32 v17, 1.0, v18
	v_rcp_f32_e32 v17, v17
	v_mul_f32_e32 v7, v8, v9
	v_mul_f32_e32 v6, v16, v6
	v_mul_f32_e32 v8, 4.0, v10
	v_mul_f32_e32 v7, v17, v7
	v_mul_f32_e32 v9, 4.0, v11
	v_mul_f32_e32 v10, 4.0, v12
	v_mul_f32_e32 v11, 4.0, v13
	v_mul_f32_e32 v12, 4.0, v14
	v_mul_f32_e32 v13, 4.0, v15
	v_mul_f32_e32 v14, 4.0, v6
	v_mul_f32_e32 v15, 4.0, v7
	v_med3_f32 v7, v8, s41, v205
	v_med3_f32 v8, v9, s41, v205
	v_mov_b32_e32 v6, v163
	v_cvt_pk_fp8_f32 v6, v7, v8
	v_med3_f32 v8, v10, s41, v205
	v_med3_f32 v9, v11, s41, v205
	v_med3_f32 v10, v12, s41, v205
	v_med3_f32 v11, v13, s41, v205
	v_mov_b32_e32 v7, v163
	v_cvt_pk_fp8_f32 v7, v10, v11
	v_cvt_pk_fp8_f32 v6, v8, v9 op_sel:[0,0,1]
	v_med3_f32 v8, v14, s41, v205
	v_med3_f32 v9, v15, s41, v205
	v_cvt_pk_fp8_f32 v7, v8, v9 op_sel:[0,0,1]
	v_mov_b32_e32 v8, v94
	v_mov_b32_e32 v9, v90
	v_pk_mul_f32 v[8:9], v[8:9], s[18:19] op_sel_hi:[1,0]
	v_mov_b32_e32 v90, v95
	v_mul_f32_e32 v10, 0xbfb8aa3b, v8
	v_exp_f32_e32 v12, v10
	v_pk_mul_f32 v[10:11], v[90:91], s[18:19] op_sel_hi:[1,0]
	v_ashrrev_i32_e32 v5, 31, v4
	v_mul_f32_e32 v13, 0xbfb8aa3b, v10
	v_lshlrev_b64 v[4:5], 11, v[4:5]
	v_exp_f32_e32 v13, v13
	v_lshl_add_u64 v[4:5], s[12:13], 0, v[4:5]
	v_lshl_add_u64 v[4:5], v[4:5], 0, v[162:163]
	global_store_dwordx2 v[4:5], v[6:7], off
	v_add_f32_e32 v4, 1.0, v12
	v_rcp_f32_e32 v4, v4
	v_add_f32_e32 v5, 1.0, v13
	v_rcp_f32_e32 v5, v5
	v_mul_f32_e32 v6, v8, v9
	v_mul_f32_e32 v8, v4, v6
	v_mul_f32_e32 v4, v10, v11
	v_mul_f32_e32 v9, v5, v4
	v_mov_b32_e32 v4, v96
	v_mov_b32_e32 v5, v92
	v_pk_mul_f32 v[4:5], v[4:5], s[18:19] op_sel_hi:[1,0]
	v_mov_b32_e32 v92, v97
	v_mul_f32_e32 v6, 0xbfb8aa3b, v4
	v_exp_f32_e32 v10, v6
	v_pk_mul_f32 v[6:7], v[92:93], s[18:19] op_sel_hi:[1,0]
	v_mul_f32_e32 v12, v4, v5
	v_mul_f32_e32 v11, 0xbfb8aa3b, v6
	v_exp_f32_e32 v11, v11
	v_add_f32_e32 v4, 1.0, v10
	v_rcp_f32_e32 v10, v4
	v_mov_b32_e32 v5, v82
	v_add_f32_e32 v4, 1.0, v11
	v_rcp_f32_e32 v11, v4
	v_mov_b32_e32 v4, v86
	v_pk_mul_f32 v[4:5], v[4:5], s[18:19] op_sel_hi:[1,0]
	v_mul_f32_e32 v6, v6, v7
	v_mul_f32_e32 v13, 0xbfb8aa3b, v4
	v_exp_f32_e32 v13, v13
	v_mul_f32_e32 v11, v11, v6
	v_mov_b32_e32 v82, v87
	v_mul_f32_e32 v10, v10, v12
	v_add_f32_e32 v6, 1.0, v13
	v_rcp_f32_e32 v12, v6
	v_pk_mul_f32 v[6:7], v[82:83], s[18:19] op_sel_hi:[1,0]
	v_mul_f32_e32 v4, v4, v5
	v_mul_f32_e32 v13, 0xbfb8aa3b, v6
	v_exp_f32_e32 v13, v13
	v_mul_f32_e32 v12, v12, v4
	v_mov_b32_e32 v5, v84
	v_mul_f32_e32 v14, v6, v7
	v_add_f32_e32 v4, 1.0, v13
	v_rcp_f32_e32 v13, v4
	v_mov_b32_e32 v4, v88
	v_pk_mul_f32 v[4:5], v[4:5], s[18:19] op_sel_hi:[1,0]
	v_mov_b32_e32 v84, v89
	v_mul_f32_e32 v6, 0xbfb8aa3b, v4
	v_exp_f32_e32 v15, v6
	v_pk_mul_f32 v[6:7], v[84:85], s[18:19] op_sel_hi:[1,0]
	v_mul_f32_e32 v13, v13, v14
	v_mul_f32_e32 v16, 0xbfb8aa3b, v6
	v_exp_f32_e32 v16, v16
	v_add_f32_e32 v14, 1.0, v15
	v_rcp_f32_e32 v14, v14
	v_mul_f32_e32 v4, v4, v5
	v_add_f32_e32 v15, 1.0, v16
	v_rcp_f32_e32 v15, v15
	v_mul_f32_e32 v5, v6, v7
	v_mul_f32_e32 v4, v14, v4
	v_mul_f32_e32 v6, 4.0, v8
	v_mul_f32_e32 v5, v15, v5
	v_mul_f32_e32 v7, 4.0, v9
	v_mul_f32_e32 v8, 4.0, v10
	v_mul_f32_e32 v9, 4.0, v11
	v_mul_f32_e32 v10, 4.0, v12
	v_mul_f32_e32 v11, 4.0, v13
	v_mul_f32_e32 v12, 4.0, v4
	v_mul_f32_e32 v13, 4.0, v5
	v_med3_f32 v5, v6, s41, v205
	v_med3_f32 v6, v7, s41, v205
	v_mov_b32_e32 v4, v163
	v_cvt_pk_fp8_f32 v4, v5, v6
	v_med3_f32 v6, v8, s41, v205
	v_med3_f32 v7, v9, s41, v205
	v_med3_f32 v8, v10, s41, v205
	v_med3_f32 v9, v11, s41, v205
	v_mov_b32_e32 v5, v163
	v_cvt_pk_fp8_f32 v5, v8, v9
	v_mov_b32_e32 v8, v78
	v_mov_b32_e32 v9, v74
	v_pk_mul_f32 v[8:9], v[8:9], s[18:19] op_sel_hi:[1,0]
	v_mov_b32_e32 v74, v79
	v_mul_f32_e32 v10, 0xbfb8aa3b, v8
	v_cvt_pk_fp8_f32 v4, v6, v7 op_sel:[0,0,1]
	v_med3_f32 v6, v12, s41, v205
	v_med3_f32 v7, v13, s41, v205
	v_exp_f32_e32 v12, v10
	v_pk_mul_f32 v[10:11], v[74:75], s[18:19] op_sel_hi:[1,0]
	v_cvt_pk_fp8_f32 v5, v6, v7 op_sel:[0,0,1]
	v_mul_f32_e32 v13, 0xbfb8aa3b, v10
	v_exp_f32_e32 v13, v13
	v_add_co_u32_e32 v6, vcc, s42, v2
	v_mov_b32_e32 v182, v176
	s_nop 0
	v_addc_co_u32_e32 v7, vcc, 0, v3, vcc
	global_store_dwordx2 v[6:7], v[4:5], off
	v_add_f32_e32 v4, 1.0, v12
	v_rcp_f32_e32 v4, v4
	v_add_f32_e32 v5, 1.0, v13
	v_rcp_f32_e32 v5, v5
	v_mul_f32_e32 v6, v8, v9
	v_mul_f32_e32 v8, v4, v6
	v_mul_f32_e32 v4, v10, v11
	v_mul_f32_e32 v9, v5, v4
	v_mov_b32_e32 v4, v80
	v_mov_b32_e32 v5, v76
	v_pk_mul_f32 v[4:5], v[4:5], s[18:19] op_sel_hi:[1,0]
	v_mov_b32_e32 v76, v81
	v_mul_f32_e32 v6, 0xbfb8aa3b, v4
	v_exp_f32_e32 v10, v6
	v_pk_mul_f32 v[6:7], v[76:77], s[18:19] op_sel_hi:[1,0]
	v_mul_f32_e32 v12, v4, v5
	v_mul_f32_e32 v11, 0xbfb8aa3b, v6
	v_exp_f32_e32 v11, v11
	v_add_f32_e32 v4, 1.0, v10
	v_rcp_f32_e32 v10, v4
	v_mov_b32_e32 v5, v66
	v_add_f32_e32 v4, 1.0, v11
	v_rcp_f32_e32 v11, v4
	v_mov_b32_e32 v4, v70
	v_pk_mul_f32 v[4:5], v[4:5], s[18:19] op_sel_hi:[1,0]
	v_mul_f32_e32 v6, v6, v7
	v_mul_f32_e32 v13, 0xbfb8aa3b, v4
	v_exp_f32_e32 v13, v13
	v_mul_f32_e32 v11, v11, v6
	v_mov_b32_e32 v66, v71
	v_mul_f32_e32 v10, v10, v12
	v_add_f32_e32 v6, 1.0, v13
	v_rcp_f32_e32 v12, v6
	v_pk_mul_f32 v[6:7], v[66:67], s[18:19] op_sel_hi:[1,0]
	v_mul_f32_e32 v4, v4, v5
	v_mul_f32_e32 v13, 0xbfb8aa3b, v6
	v_exp_f32_e32 v13, v13
	v_mul_f32_e32 v12, v12, v4
	v_mov_b32_e32 v5, v68
	v_mul_f32_e32 v14, v6, v7
	v_add_f32_e32 v4, 1.0, v13
	v_rcp_f32_e32 v13, v4
	v_mov_b32_e32 v4, v72
	v_pk_mul_f32 v[4:5], v[4:5], s[18:19] op_sel_hi:[1,0]
	v_mov_b32_e32 v68, v73
	v_mul_f32_e32 v6, 0xbfb8aa3b, v4
	v_exp_f32_e32 v15, v6
	v_pk_mul_f32 v[6:7], v[68:69], s[18:19] op_sel_hi:[1,0]
	v_mul_f32_e32 v13, v13, v14
	v_mul_f32_e32 v16, 0xbfb8aa3b, v6
	v_exp_f32_e32 v16, v16
	v_add_f32_e32 v14, 1.0, v15
	v_rcp_f32_e32 v14, v14
	v_mul_f32_e32 v4, v4, v5
	v_add_f32_e32 v15, 1.0, v16
	v_rcp_f32_e32 v15, v15
	v_mul_f32_e32 v5, v6, v7
	v_mul_f32_e32 v4, v14, v4
	v_mul_f32_e32 v6, 4.0, v8
	v_mul_f32_e32 v5, v15, v5
	v_mul_f32_e32 v7, 4.0, v9
	v_mul_f32_e32 v8, 4.0, v10
	v_mul_f32_e32 v9, 4.0, v11
	v_mul_f32_e32 v10, 4.0, v12
	v_mul_f32_e32 v11, 4.0, v13
	v_mul_f32_e32 v12, 4.0, v4
	v_mul_f32_e32 v13, 4.0, v5
	v_med3_f32 v5, v6, s41, v205
	v_med3_f32 v6, v7, s41, v205
	v_mov_b32_e32 v4, v163
	v_cvt_pk_fp8_f32 v4, v5, v6
	v_med3_f32 v6, v8, s41, v205
	v_med3_f32 v7, v9, s41, v205
	v_med3_f32 v8, v10, s41, v205
	v_med3_f32 v9, v11, s41, v205
	v_mov_b32_e32 v5, v163
	v_cvt_pk_fp8_f32 v5, v8, v9
	v_mov_b32_e32 v8, v62
	v_mov_b32_e32 v9, v58
	v_pk_mul_f32 v[8:9], v[8:9], s[18:19] op_sel_hi:[1,0]
	v_mov_b32_e32 v58, v63
	v_mul_f32_e32 v10, 0xbfb8aa3b, v8
	v_cvt_pk_fp8_f32 v4, v6, v7 op_sel:[0,0,1]
	v_med3_f32 v6, v12, s41, v205
	v_med3_f32 v7, v13, s41, v205
	v_exp_f32_e32 v12, v10
	v_pk_mul_f32 v[10:11], v[58:59], s[18:19] op_sel_hi:[1,0]
	v_cvt_pk_fp8_f32 v5, v6, v7 op_sel:[0,0,1]
	v_mul_f32_e32 v13, 0xbfb8aa3b, v10
	v_exp_f32_e32 v13, v13
	v_add_co_u32_e32 v6, vcc, s43, v2
	v_mov_b32_e32 v180, v174
	s_nop 0
	v_addc_co_u32_e32 v7, vcc, 0, v3, vcc
	global_store_dwordx2 v[6:7], v[4:5], off
	v_add_f32_e32 v4, 1.0, v12
	v_rcp_f32_e32 v4, v4
	v_add_f32_e32 v5, 1.0, v13
	v_rcp_f32_e32 v5, v5
	v_mul_f32_e32 v6, v8, v9
	v_mul_f32_e32 v8, v4, v6
	v_mul_f32_e32 v4, v10, v11
	v_mul_f32_e32 v9, v5, v4
	v_mov_b32_e32 v4, v64
	v_mov_b32_e32 v5, v60
	v_pk_mul_f32 v[4:5], v[4:5], s[18:19] op_sel_hi:[1,0]
	v_mov_b32_e32 v60, v65
	v_mul_f32_e32 v6, 0xbfb8aa3b, v4
	v_exp_f32_e32 v10, v6
	v_pk_mul_f32 v[6:7], v[60:61], s[18:19] op_sel_hi:[1,0]
	v_mul_f32_e32 v12, v4, v5
	v_mul_f32_e32 v11, 0xbfb8aa3b, v6
	v_exp_f32_e32 v11, v11
	v_add_f32_e32 v4, 1.0, v10
	v_rcp_f32_e32 v10, v4
	v_mov_b32_e32 v5, v50
	v_add_f32_e32 v4, 1.0, v11
	v_rcp_f32_e32 v11, v4
	v_mov_b32_e32 v4, v54
	v_pk_mul_f32 v[4:5], v[4:5], s[18:19] op_sel_hi:[1,0]
	v_mul_f32_e32 v6, v6, v7
	v_mul_f32_e32 v13, 0xbfb8aa3b, v4
	v_exp_f32_e32 v13, v13
	v_mul_f32_e32 v11, v11, v6
	v_mov_b32_e32 v50, v55
	v_mul_f32_e32 v10, v10, v12
	v_add_f32_e32 v6, 1.0, v13
	v_rcp_f32_e32 v12, v6
	v_pk_mul_f32 v[6:7], v[50:51], s[18:19] op_sel_hi:[1,0]
	v_mul_f32_e32 v4, v4, v5
	v_mul_f32_e32 v13, 0xbfb8aa3b, v6
	v_exp_f32_e32 v13, v13
	v_mul_f32_e32 v12, v12, v4
	v_mov_b32_e32 v5, v52
	v_mul_f32_e32 v14, v6, v7
	v_add_f32_e32 v4, 1.0, v13
	v_rcp_f32_e32 v13, v4
	v_mov_b32_e32 v4, v56
	v_pk_mul_f32 v[4:5], v[4:5], s[18:19] op_sel_hi:[1,0]
	v_mov_b32_e32 v52, v57
	v_mul_f32_e32 v6, 0xbfb8aa3b, v4
	v_exp_f32_e32 v15, v6
	v_pk_mul_f32 v[6:7], v[52:53], s[18:19] op_sel_hi:[1,0]
	v_mul_f32_e32 v13, v13, v14
	v_mul_f32_e32 v16, 0xbfb8aa3b, v6
	v_exp_f32_e32 v16, v16
	v_add_f32_e32 v14, 1.0, v15
	v_rcp_f32_e32 v14, v14
	v_mul_f32_e32 v4, v4, v5
	v_add_f32_e32 v15, 1.0, v16
	v_rcp_f32_e32 v15, v15
	v_mul_f32_e32 v5, v6, v7
	v_mul_f32_e32 v4, v14, v4
	v_mul_f32_e32 v6, 4.0, v8
	v_mul_f32_e32 v5, v15, v5
	v_mul_f32_e32 v7, 4.0, v9
	v_mul_f32_e32 v8, 4.0, v10
	v_mul_f32_e32 v9, 4.0, v11
	v_mul_f32_e32 v10, 4.0, v12
	v_mul_f32_e32 v11, 4.0, v13
	v_mul_f32_e32 v12, 4.0, v4
	v_mul_f32_e32 v13, 4.0, v5
	v_med3_f32 v5, v6, s41, v205
	v_med3_f32 v6, v7, s41, v205
	v_mov_b32_e32 v4, v163
	v_cvt_pk_fp8_f32 v4, v5, v6
	v_med3_f32 v6, v8, s41, v205
	v_med3_f32 v7, v9, s41, v205
	v_med3_f32 v8, v10, s41, v205
	v_med3_f32 v9, v11, s41, v205
	v_mov_b32_e32 v5, v163
	v_cvt_pk_fp8_f32 v5, v8, v9
	v_mov_b32_e32 v8, v46
	v_mov_b32_e32 v9, v42
	v_pk_mul_f32 v[8:9], v[8:9], s[18:19] op_sel_hi:[1,0]
	v_mov_b32_e32 v42, v47
	v_mul_f32_e32 v10, 0xbfb8aa3b, v8
	v_cvt_pk_fp8_f32 v4, v6, v7 op_sel:[0,0,1]
	v_med3_f32 v6, v12, s41, v205
	v_med3_f32 v7, v13, s41, v205
	v_exp_f32_e32 v12, v10
	v_pk_mul_f32 v[10:11], v[42:43], s[18:19] op_sel_hi:[1,0]
	v_cvt_pk_fp8_f32 v5, v6, v7 op_sel:[0,0,1]
	v_mul_f32_e32 v13, 0xbfb8aa3b, v10
	v_exp_f32_e32 v13, v13
	v_add_co_u32_e32 v6, vcc, s44, v2
	v_mov_b32_e32 v178, v207
	s_nop 0
	v_addc_co_u32_e32 v7, vcc, 0, v3, vcc
	global_store_dwordx2 v[6:7], v[4:5], off
	v_add_f32_e32 v4, 1.0, v12
	v_rcp_f32_e32 v4, v4
	v_add_f32_e32 v5, 1.0, v13
	v_rcp_f32_e32 v5, v5
	v_mul_f32_e32 v6, v8, v9
	v_mul_f32_e32 v8, v4, v6
	v_mul_f32_e32 v4, v10, v11
	v_mul_f32_e32 v9, v5, v4
	v_mov_b32_e32 v4, v48
	v_mov_b32_e32 v5, v44
	v_pk_mul_f32 v[4:5], v[4:5], s[18:19] op_sel_hi:[1,0]
	v_mov_b32_e32 v44, v49
	v_mul_f32_e32 v6, 0xbfb8aa3b, v4
	v_exp_f32_e32 v10, v6
	v_pk_mul_f32 v[6:7], v[44:45], s[18:19] op_sel_hi:[1,0]
	v_mul_f32_e32 v12, v4, v5
	v_mul_f32_e32 v11, 0xbfb8aa3b, v6
	v_exp_f32_e32 v11, v11
	v_add_f32_e32 v4, 1.0, v10
	v_rcp_f32_e32 v10, v4
	v_mov_b32_e32 v5, v34
	v_add_f32_e32 v4, 1.0, v11
	v_rcp_f32_e32 v11, v4
	v_mov_b32_e32 v4, v38
	v_pk_mul_f32 v[4:5], v[4:5], s[18:19] op_sel_hi:[1,0]
	v_mul_f32_e32 v6, v6, v7
	v_mul_f32_e32 v13, 0xbfb8aa3b, v4
	v_exp_f32_e32 v13, v13
	v_mul_f32_e32 v11, v11, v6
	v_mov_b32_e32 v34, v39
	v_mul_f32_e32 v10, v10, v12
	v_add_f32_e32 v6, 1.0, v13
	v_rcp_f32_e32 v12, v6
	v_pk_mul_f32 v[6:7], v[34:35], s[18:19] op_sel_hi:[1,0]
	v_mul_f32_e32 v4, v4, v5
	v_mul_f32_e32 v13, 0xbfb8aa3b, v6
	v_exp_f32_e32 v13, v13
	v_mul_f32_e32 v12, v12, v4
	v_mov_b32_e32 v5, v36
	v_mul_f32_e32 v14, v6, v7
	v_add_f32_e32 v4, 1.0, v13
	v_rcp_f32_e32 v13, v4
	v_mov_b32_e32 v4, v40
	v_pk_mul_f32 v[4:5], v[4:5], s[18:19] op_sel_hi:[1,0]
	v_mov_b32_e32 v36, v41
	v_mul_f32_e32 v6, 0xbfb8aa3b, v4
	v_exp_f32_e32 v15, v6
	v_pk_mul_f32 v[6:7], v[36:37], s[18:19] op_sel_hi:[1,0]
	v_mul_f32_e32 v13, v13, v14
	v_mul_f32_e32 v16, 0xbfb8aa3b, v6
	v_exp_f32_e32 v16, v16
	v_add_f32_e32 v14, 1.0, v15
	v_rcp_f32_e32 v14, v14
	v_mul_f32_e32 v4, v4, v5
	v_add_f32_e32 v15, 1.0, v16
	v_rcp_f32_e32 v15, v15
	v_mul_f32_e32 v5, v6, v7
	v_mul_f32_e32 v4, v14, v4
	v_mul_f32_e32 v6, 4.0, v8
	v_mul_f32_e32 v5, v15, v5
	v_mul_f32_e32 v7, 4.0, v9
	v_mul_f32_e32 v8, 4.0, v10
	v_mul_f32_e32 v9, 4.0, v11
	v_mul_f32_e32 v10, 4.0, v12
	v_mul_f32_e32 v11, 4.0, v13
	v_mul_f32_e32 v12, 4.0, v4
	v_mul_f32_e32 v13, 4.0, v5
	v_med3_f32 v5, v6, s41, v205
	v_med3_f32 v6, v7, s41, v205
	v_mov_b32_e32 v4, v163
	v_cvt_pk_fp8_f32 v4, v5, v6
	v_med3_f32 v6, v8, s41, v205
	v_med3_f32 v7, v9, s41, v205
	v_med3_f32 v8, v10, s41, v205
	v_med3_f32 v9, v11, s41, v205
	v_mov_b32_e32 v5, v163
	v_cvt_pk_fp8_f32 v5, v8, v9
	v_cvt_pk_fp8_f32 v4, v6, v7 op_sel:[0,0,1]
	v_med3_f32 v6, v12, s41, v205
	v_med3_f32 v7, v13, s41, v205
	v_cvt_pk_fp8_f32 v5, v6, v7 op_sel:[0,0,1]
	v_add_co_u32_e32 v2, vcc, 0x58000, v2
	v_mov_b32_e32 v208, v206
	s_nop 0
	v_addc_co_u32_e32 v3, vcc, 0, v3, vcc
	s_and_b64 vcc, exec, s[0:1]
	s_mov_b32 s48, s47
	s_mov_b32 s22, s20
	s_mov_b64 s[24:25], s[6:7]
	s_mov_b32 s21, s45
	global_store_dwordx2 v[2:3], v[4:5], off
	s_cbranch_vccz .LBB0_1042
	s_waitcnt vmcnt(0)
	s_cmpk_gt_u32 s19, 0xff
	s_cbranch_scc1 .LBB0_1064
	s_barrier

.LBB0_1127:
	s_ashr_i32 s19, s18, 31
	s_lshl_b64 s[22:23], s[18:19], 19
	s_add_u32 s22, s38, s22
	s_addc_u32 s23, s39, s23
	s_and_b64 s[24:25], s[0:1], exec
	s_cselect_b32 s19, s23, s31
	s_cselect_b32 s56, s22, s30
	s_ashr_i32 s21, s20, 31
	s_lshl_b64 s[24:25], s[20:21], 19
	s_add_u32 s24, s40, s24
	s_addc_u32 s25, s41, s25
	s_and_b64 s[36:37], s[0:1], exec
	s_cselect_b32 s21, s25, s35
	s_cselect_b32 s57, s24, s34
	s_add_u32 s30, s30, 0x40080
	s_addc_u32 s31, s31, 0
	s_add_u32 s58, s34, 0x100
	v_mov_b32_e32 v18, 0
	s_addc_u32 s59, s35, 0
	s_mov_b32 s60, -2
	v_mov_b32_e32 v19, v18
	v_mov_b32_e32 v20, v18
	v_mov_b32_e32 v21, v18
	v_mov_b32_e32 v22, v18
	v_mov_b32_e32 v23, v18
	v_mov_b32_e32 v24, v18
	v_mov_b32_e32 v25, v18
	v_mov_b32_e32 v30, v18
	v_mov_b32_e32 v31, v18
	v_mov_b32_e32 v32, v18
	v_mov_b32_e32 v33, v18
	v_mov_b32_e32 v38, v18
	v_mov_b32_e32 v39, v18
	v_mov_b32_e32 v40, v18
	v_mov_b32_e32 v41, v18
	v_mov_b32_e32 v46, v18
	v_mov_b32_e32 v47, v18
	v_mov_b32_e32 v48, v18
	v_mov_b32_e32 v49, v18
	v_mov_b32_e32 v54, v18
	v_mov_b32_e32 v55, v18
	v_mov_b32_e32 v56, v18
	v_mov_b32_e32 v57, v18
	v_mov_b32_e32 v62, v18
	v_mov_b32_e32 v63, v18
	v_mov_b32_e32 v64, v18
	v_mov_b32_e32 v65, v18
	v_mov_b32_e32 v70, v18
	v_mov_b32_e32 v71, v18
	v_mov_b32_e32 v72, v18
	v_mov_b32_e32 v73, v18
	v_mov_b32_e32 v26, v18
	v_mov_b32_e32 v27, v18
	v_mov_b32_e32 v28, v18
	v_mov_b32_e32 v29, v18
	v_mov_b32_e32 v34, v18
	v_mov_b32_e32 v35, v18
	v_mov_b32_e32 v36, v18
	v_mov_b32_e32 v37, v18
	v_mov_b32_e32 v42, v18
	v_mov_b32_e32 v43, v18
	v_mov_b32_e32 v44, v18
	v_mov_b32_e32 v45, v18
	v_mov_b32_e32 v50, v18
	v_mov_b32_e32 v51, v18
	v_mov_b32_e32 v52, v18
	v_mov_b32_e32 v53, v18
	v_mov_b32_e32 v58, v18
	v_mov_b32_e32 v59, v18
	v_mov_b32_e32 v60, v18
	v_mov_b32_e32 v61, v18
	v_mov_b32_e32 v66, v18
	v_mov_b32_e32 v67, v18
	v_mov_b32_e32 v68, v18
	v_mov_b32_e32 v69, v18
	v_mov_b32_e32 v74, v18
	v_mov_b32_e32 v75, v18
	v_mov_b32_e32 v76, v18
	v_mov_b32_e32 v77, v18
	v_mov_b32_e32 v78, v18
	v_mov_b32_e32 v79, v18
	v_mov_b32_e32 v80, v18
	v_mov_b32_e32 v81, v18
	v_mov_b32_e32 v82, v18
	v_mov_b32_e32 v83, v18
	v_mov_b32_e32 v84, v18
	v_mov_b32_e32 v85, v18
	v_mov_b32_e32 v86, v18
	v_mov_b32_e32 v87, v18
	v_mov_b32_e32 v88, v18
	v_mov_b32_e32 v89, v18
	v_mov_b32_e32 v98, v18
	v_mov_b32_e32 v99, v18
	v_mov_b32_e32 v100, v18
	v_mov_b32_e32 v101, v18
	v_mov_b32_e32 v102, v18
	v_mov_b32_e32 v103, v18
	v_mov_b32_e32 v104, v18
	v_mov_b32_e32 v105, v18
	v_mov_b32_e32 v114, v18
	v_mov_b32_e32 v115, v18
	v_mov_b32_e32 v116, v18
	v_mov_b32_e32 v117, v18
	v_mov_b32_e32 v118, v18
	v_mov_b32_e32 v119, v18
	v_mov_b32_e32 v120, v18
	v_mov_b32_e32 v121, v18
	v_mov_b32_e32 v130, v18
	v_mov_b32_e32 v131, v18
	v_mov_b32_e32 v132, v18
	v_mov_b32_e32 v133, v18
	v_mov_b32_e32 v134, v18
	v_mov_b32_e32 v135, v18
	v_mov_b32_e32 v136, v18
	v_mov_b32_e32 v137, v18
	v_mov_b32_e32 v90, v18
	v_mov_b32_e32 v91, v18
	v_mov_b32_e32 v92, v18
	v_mov_b32_e32 v93, v18
	v_mov_b32_e32 v94, v18
	v_mov_b32_e32 v95, v18
	v_mov_b32_e32 v96, v18
	v_mov_b32_e32 v97, v18
	v_mov_b32_e32 v106, v18
	v_mov_b32_e32 v107, v18
	v_mov_b32_e32 v108, v18
	v_mov_b32_e32 v109, v18
	v_mov_b32_e32 v110, v18
	v_mov_b32_e32 v111, v18
	v_mov_b32_e32 v112, v18
	v_mov_b32_e32 v113, v18
	v_mov_b32_e32 v122, v18
	v_mov_b32_e32 v123, v18
	v_mov_b32_e32 v124, v18
	v_mov_b32_e32 v125, v18
	v_mov_b32_e32 v126, v18
	v_mov_b32_e32 v127, v18
	v_mov_b32_e32 v128, v18
	v_mov_b32_e32 v129, v18
	v_mov_b32_e32 v138, v18
	v_mov_b32_e32 v139, v18
	v_mov_b32_e32 v140, v18
	v_mov_b32_e32 v141, v18
	v_mov_b32_e32 v142, v18
	v_mov_b32_e32 v143, v18
	v_mov_b32_e32 v144, v18
	v_mov_b32_e32 v145, v18
	ds_read_b128 v[2:5], v176
	ds_read_b128 v[6:9], v176 offset:1024
	ds_read_b128 v[10:13], v176 offset:2048
	ds_read_b128 v[14:17], v176 offset:3072
.LBB0_1128:
	s_add_u32 s34, s30, 0xfffc0080
	s_addc_u32 s35, s31, -1
	s_cmp_eq_u32 s60, 12
	s_cselect_b32 s37, s19, s35
	s_cselect_b32 s36, s56, s34
	s_cselect_b32 s35, s21, s59
	s_cselect_b32 s34, s57, s58
	v_lshl_add_u64 v[164:165], s[30:31], 0, v[156:157]
	s_add_i32 m0, s27, 0xc000
	ds_read_b128 v[184:187], v177
	ds_read_b128 v[188:191], v177 offset:1024
	ds_read_b128 v[198:201], v177 offset:2048
	ds_read_b128 v[202:205], v177 offset:3072
	ds_read_b128 v[206:209], v177 offset:4096
	ds_read_b128 v[210:213], v177 offset:5120
	ds_read_b128 v[214:217], v177 offset:6144
	ds_read_b128 v[218:221], v177 offset:7168
	global_load_lds_dwordx4 v[164:165], off
	v_lshl_add_u64 v[164:165], s[30:31], 0, v[158:159]
	s_add_i32 m0, s27, 0xe000
	s_nop 0
	global_load_lds_dwordx4 v[164:165], off
	s_waitcnt lgkmcnt(8)
	s_barrier
	s_waitcnt lgkmcnt(0)
	s_waitcnt lgkmcnt(0)
	v_mfma_f32_16x16x128_f8f6f4 v[142:145], v[2:9], v[184:191], v[142:145]
	v_mfma_f32_16x16x128_f8f6f4 v[138:141], v[10:17], v[184:191], v[138:141]
	v_mfma_f32_16x16x128_f8f6f4 v[126:129], v[2:9], v[198:205], v[126:129]
	v_mfma_f32_16x16x128_f8f6f4 v[122:125], v[10:17], v[198:205], v[122:125]
	v_mfma_f32_16x16x128_f8f6f4 v[110:113], v[2:9], v[206:213], v[110:113]
	v_mfma_f32_16x16x128_f8f6f4 v[106:109], v[10:17], v[206:213], v[106:109]
	v_mfma_f32_16x16x128_f8f6f4 v[94:97], v[2:9], v[214:221], v[94:97]
	v_mfma_f32_16x16x128_f8f6f4 v[90:93], v[10:17], v[214:221], v[90:93]
	s_barrier
	s_add_i32 s61, s50, s42
	v_lshl_add_u64 v[164:165], s[34:35], 0, v[148:149]
	s_mov_b32 m0, s61
	ds_read_b128 v[222:225], v178
	ds_read_b128 v[226:229], v178 offset:1024
	ds_read_b128 v[230:233], v178 offset:2048
	ds_read_b128 v[234:237], v178 offset:3072
	global_load_lds_dwordx4 v[164:165], off
	v_lshl_add_u64 v[166:167], s[34:35], 0, v[152:153]
	s_add_i32 m0, s61, 0x2000
	s_nop 0
	global_load_lds_dwordx4 v[166:167], off
	s_barrier
	s_waitcnt lgkmcnt(0)
	s_waitcnt lgkmcnt(0)
	v_mfma_f32_16x16x128_f8f6f4 v[134:137], v[222:229], v[184:191], v[134:137]
	v_mfma_f32_16x16x128_f8f6f4 v[130:133], v[230:237], v[184:191], v[130:133]
	v_mfma_f32_16x16x128_f8f6f4 v[118:121], v[222:229], v[198:205], v[118:121]
	v_mfma_f32_16x16x128_f8f6f4 v[114:117], v[230:237], v[198:205], v[114:117]
	v_mfma_f32_16x16x128_f8f6f4 v[102:105], v[222:229], v[206:213], v[102:105]
	v_mfma_f32_16x16x128_f8f6f4 v[98:101], v[230:237], v[206:213], v[98:101]
	v_mfma_f32_16x16x128_f8f6f4 v[86:89], v[222:229], v[214:221], v[86:89]
	v_mfma_f32_16x16x128_f8f6f4 v[82:85], v[230:237], v[214:221], v[82:85]
	s_mov_b32 m0, s27
	v_lshl_add_u64 v[168:169], s[36:37], 0, v[146:147]
	s_barrier
	ds_read_b128 v[184:187], v177 offset:16384
	ds_read_b128 v[188:191], v177 offset:17408
	ds_read_b128 v[198:201], v177 offset:18432
	ds_read_b128 v[202:205], v177 offset:19456
	ds_read_b128 v[206:209], v177 offset:20480
	ds_read_b128 v[210:213], v177 offset:21504
	ds_read_b128 v[214:217], v177 offset:22528
	ds_read_b128 v[218:221], v177 offset:23552
	global_load_lds_dwordx4 v[168:169], off
	v_lshl_add_u64 v[170:171], s[36:37], 0, v[150:151]
	s_mov_b32 m0, s29
	s_nop 0
	global_load_lds_dwordx4 v[170:171], off
	s_waitcnt vmcnt(10)
	s_barrier
	s_waitcnt lgkmcnt(0)
	s_waitcnt lgkmcnt(0)
	v_mfma_f32_16x16x128_f8f6f4 v[78:81], v[2:9], v[184:191], v[78:81]
	v_mfma_f32_16x16x128_f8f6f4 v[74:77], v[10:17], v[184:191], v[74:77]
	v_mfma_f32_16x16x128_f8f6f4 v[66:69], v[2:9], v[198:205], v[66:69]
	v_mfma_f32_16x16x128_f8f6f4 v[58:61], v[10:17], v[198:205], v[58:61]
	v_mfma_f32_16x16x128_f8f6f4 v[50:53], v[2:9], v[206:213], v[50:53]
	v_mfma_f32_16x16x128_f8f6f4 v[42:45], v[10:17], v[206:213], v[42:45]
	v_mfma_f32_16x16x128_f8f6f4 v[34:37], v[2:9], v[214:221], v[34:37]
	v_mfma_f32_16x16x128_f8f6f4 v[26:29], v[10:17], v[214:221], v[26:29]
	s_barrier
	ds_read_b128 v[2:5], v176 offset:32768
	ds_read_b128 v[6:9], v176 offset:33792
	ds_read_b128 v[10:13], v176 offset:34816
	ds_read_b128 v[14:17], v176 offset:35840
	s_add_u32 s64, s34, 0x40000
	s_addc_u32 s65, s35, 0
	s_add_i32 s61, s51, s42
	v_lshl_add_u64 v[238:239], s[64:65], 0, v[148:149]
	s_mov_b32 m0, s61
	s_nop 0
	global_load_lds_dwordx4 v[238:239], off
	v_lshl_add_u64 v[238:239], s[64:65], 0, v[152:153]
	s_add_i32 m0, s61, 0x2000
	s_nop 0
	global_load_lds_dwordx4 v[238:239], off
	s_waitcnt vmcnt(6)
	s_barrier
	v_mfma_f32_16x16x128_f8f6f4 v[70:73], v[222:229], v[184:191], v[70:73]
	v_mfma_f32_16x16x128_f8f6f4 v[62:65], v[230:237], v[184:191], v[62:65]
	v_mfma_f32_16x16x128_f8f6f4 v[54:57], v[222:229], v[198:205], v[54:57]
	v_mfma_f32_16x16x128_f8f6f4 v[46:49], v[230:237], v[198:205], v[46:49]
	v_mfma_f32_16x16x128_f8f6f4 v[38:41], v[222:229], v[206:213], v[38:41]
	v_mfma_f32_16x16x128_f8f6f4 v[30:33], v[230:237], v[206:213], v[30:33]
	v_mfma_f32_16x16x128_f8f6f4 v[22:25], v[222:229], v[214:221], v[22:25]
	v_mfma_f32_16x16x128_f8f6f4 v[18:21], v[230:237], v[214:221], v[18:21]
	s_add_i32 s61, 0, 0x18000
	s_barrier
	s_add_u32 s36, s36, 0x40000
	s_addc_u32 s37, s37, 0
	s_mov_b32 m0, s44
	v_lshl_add_u64 v[192:193], s[36:37], 0, v[146:147]
	ds_read_b128 v[184:187], v177 offset:32768
	ds_read_b128 v[188:191], v177 offset:33792
	ds_read_b128 v[198:201], v177 offset:34816
	ds_read_b128 v[202:205], v177 offset:35840
	ds_read_b128 v[206:209], v177 offset:36864
	ds_read_b128 v[210:213], v177 offset:37888
	ds_read_b128 v[214:217], v177 offset:38912
	ds_read_b128 v[218:221], v177 offset:39936
	global_load_lds_dwordx4 v[192:193], off
	v_lshl_add_u64 v[192:193], s[36:37], 0, v[150:151]
	s_mov_b32 m0, s45
	s_nop 0
	global_load_lds_dwordx4 v[192:193], off
	s_waitcnt lgkmcnt(8)
	s_barrier
	s_waitcnt lgkmcnt(0)
	s_waitcnt lgkmcnt(0)
	v_mfma_f32_16x16x128_f8f6f4 v[142:145], v[2:9], v[184:191], v[142:145]
	v_mfma_f32_16x16x128_f8f6f4 v[138:141], v[10:17], v[184:191], v[138:141]
	v_mfma_f32_16x16x128_f8f6f4 v[126:129], v[2:9], v[198:205], v[126:129]
	v_mfma_f32_16x16x128_f8f6f4 v[122:125], v[10:17], v[198:205], v[122:125]
	v_mfma_f32_16x16x128_f8f6f4 v[110:113], v[2:9], v[206:213], v[110:113]
	v_mfma_f32_16x16x128_f8f6f4 v[106:109], v[10:17], v[206:213], v[106:109]
	v_mfma_f32_16x16x128_f8f6f4 v[94:97], v[2:9], v[214:221], v[94:97]
	v_mfma_f32_16x16x128_f8f6f4 v[90:93], v[10:17], v[214:221], v[90:93]
	s_barrier
	s_add_i32 s36, 0, 0x1c000
	s_add_i32 s37, s61, s42
	v_add_u32_e32 v192, s36, v174
	v_lshl_add_u64 v[164:165], v[164:165], 0, s[8:9]
	s_mov_b32 m0, s37
	ds_read_b128 v[222:225], v192
	ds_read_b128 v[226:229], v192 offset:1024
	ds_read_b128 v[230:233], v192 offset:2048
	ds_read_b128 v[234:237], v192 offset:3072
	global_load_lds_dwordx4 v[164:165], off
	v_lshl_add_u64 v[164:165], v[166:167], 0, s[8:9]
	s_add_i32 m0, s37, 0x2000
	s_nop 0
	global_load_lds_dwordx4 v[164:165], off
	s_barrier
	s_waitcnt lgkmcnt(0)
	s_waitcnt lgkmcnt(0)
	v_mfma_f32_16x16x128_f8f6f4 v[134:137], v[222:229], v[184:191], v[134:137]
	v_mfma_f32_16x16x128_f8f6f4 v[130:133], v[230:237], v[184:191], v[130:133]
	v_mfma_f32_16x16x128_f8f6f4 v[118:121], v[222:229], v[198:205], v[118:121]
	v_mfma_f32_16x16x128_f8f6f4 v[114:117], v[230:237], v[198:205], v[114:117]
	v_mfma_f32_16x16x128_f8f6f4 v[102:105], v[222:229], v[206:213], v[102:105]
	v_mfma_f32_16x16x128_f8f6f4 v[98:101], v[230:237], v[206:213], v[98:101]
	v_mfma_f32_16x16x128_f8f6f4 v[86:89], v[222:229], v[214:221], v[86:89]
	v_mfma_f32_16x16x128_f8f6f4 v[82:85], v[230:237], v[214:221], v[82:85]
	s_mov_b32 m0, s48
	v_lshl_add_u64 v[164:165], v[168:169], 0, s[8:9]
	s_barrier
	ds_read_b128 v[184:187], v177 offset:49152
	ds_read_b128 v[188:191], v177 offset:50176
	ds_read_b128 v[198:201], v177 offset:51200
	ds_read_b128 v[202:205], v177 offset:52224
	ds_read_b128 v[206:209], v177 offset:53248
	ds_read_b128 v[210:213], v177 offset:54272
	ds_read_b128 v[214:217], v177 offset:55296
	ds_read_b128 v[218:221], v177 offset:56320
	global_load_lds_dwordx4 v[164:165], off
	v_lshl_add_u64 v[164:165], v[170:171], 0, s[8:9]
	s_mov_b32 m0, s49
	s_nop 0
	global_load_lds_dwordx4 v[164:165], off
	s_waitcnt vmcnt(10)
	s_barrier
	s_waitcnt lgkmcnt(0)
	s_waitcnt lgkmcnt(0)
	v_mfma_f32_16x16x128_f8f6f4 v[78:81], v[2:9], v[184:191], v[78:81]
	v_mfma_f32_16x16x128_f8f6f4 v[74:77], v[10:17], v[184:191], v[74:77]
	v_mfma_f32_16x16x128_f8f6f4 v[66:69], v[2:9], v[198:205], v[66:69]
	v_mfma_f32_16x16x128_f8f6f4 v[58:61], v[10:17], v[198:205], v[58:61]
	v_mfma_f32_16x16x128_f8f6f4 v[50:53], v[2:9], v[206:213], v[50:53]
	v_mfma_f32_16x16x128_f8f6f4 v[42:45], v[10:17], v[206:213], v[42:45]
	v_mfma_f32_16x16x128_f8f6f4 v[34:37], v[2:9], v[214:221], v[34:37]
	v_mfma_f32_16x16x128_f8f6f4 v[26:29], v[10:17], v[214:221], v[26:29]
	s_barrier
	ds_read_b128 v[2:5], v176
	ds_read_b128 v[6:9], v176 offset:1024
	ds_read_b128 v[10:13], v176 offset:2048
	ds_read_b128 v[14:17], v176 offset:3072
	s_add_u32 s34, s34, 0x40080
	s_addc_u32 s35, s35, 0
	s_add_i32 s36, s36, s42
	v_lshl_add_u64 v[238:239], s[34:35], 0, v[148:149]
	s_mov_b32 m0, s36
	s_nop 0
	global_load_lds_dwordx4 v[238:239], off
	v_lshl_add_u64 v[238:239], s[34:35], 0, v[152:153]
	s_add_i32 m0, s36, 0x2000
	s_nop 0
	global_load_lds_dwordx4 v[238:239], off
	s_waitcnt vmcnt(6)
	s_barrier
	v_mfma_f32_16x16x128_f8f6f4 v[70:73], v[222:229], v[184:191], v[70:73]
	v_mfma_f32_16x16x128_f8f6f4 v[62:65], v[230:237], v[184:191], v[62:65]
	v_mfma_f32_16x16x128_f8f6f4 v[54:57], v[222:229], v[198:205], v[54:57]
	v_mfma_f32_16x16x128_f8f6f4 v[46:49], v[230:237], v[198:205], v[46:49]
	v_mfma_f32_16x16x128_f8f6f4 v[38:41], v[222:229], v[206:213], v[38:41]
	v_mfma_f32_16x16x128_f8f6f4 v[30:33], v[230:237], v[206:213], v[30:33]
	v_mfma_f32_16x16x128_f8f6f4 v[22:25], v[222:229], v[214:221], v[22:25]
	v_mfma_f32_16x16x128_f8f6f4 v[18:21], v[230:237], v[214:221], v[18:21]
	s_add_i32 s60, s60, 2
	s_add_u32 s30, s30, 0x100
	s_addc_u32 s31, s31, 0
	s_add_u32 s58, s58, 0x100
	s_addc_u32 s59, s59, 0
	s_cmp_gt_u32 s60, 13
	s_barrier
	s_cbranch_scc0 .LBB0_1128
	s_waitcnt lgkmcnt(0)
	v_lshl_add_u32 v8, s26, 8, v172
	s_lshl_b32 s19, s28, 8
	s_and_b32 s19, s19, 0x700
	v_ashrrev_i32_e32 v9, 31, v8
	v_or_b32_e32 v4, s19, v175
	s_waitcnt vmcnt(0)
	v_mul_f32_e32 v10, 0x3b800000, v154
	v_lshlrev_b64 v[2:3], 12, v[8:9]
	v_lshl_add_u64 v[2:3], s[6:7], 0, v[2:3]
	v_lshlrev_b32_e32 v154, 1, v4
	v_pk_mul_f32 v[4:5], v[10:11], v[142:143] op_sel_hi:[0,1]
	s_nop 15
	s_nop 15
	v_lshl_add_u64 v[2:3], v[2:3], 0, v[154:155]
	v_pk_mul_f32 v[6:7], v[10:11], v[144:145] op_sel_hi:[0,1]
	v_cvt_pk_bf16_f32 v4, v4, v5
	v_cvt_pk_bf16_f32 v5, v6, v7
	v_pk_mul_f32 v[12:13], v[10:11], v[140:141] op_sel_hi:[0,1]
	v_pk_mul_f32 v[14:15], v[10:11], v[138:139] op_sel_hi:[0,1]
	v_cvt_pk_bf16_f32 v6, v14, v15
	v_cvt_pk_bf16_f32 v7, v12, v13
	global_store_dwordx4 v[2:3], v[4:7], off
	v_pk_mul_f32 v[12:13], v[10:11], v[132:133] op_sel_hi:[0,1]
	s_nop 0
	v_pk_mul_f32 v[4:5], v[10:11], v[134:135] op_sel_hi:[0,1]
	v_pk_mul_f32 v[6:7], v[10:11], v[136:137] op_sel_hi:[0,1]
	v_cvt_pk_bf16_f32 v4, v4, v5
	v_pk_mul_f32 v[10:11], v[10:11], v[130:131] op_sel_hi:[0,1]
	v_cvt_pk_bf16_f32 v5, v6, v7
	v_cvt_pk_bf16_f32 v6, v10, v11
	v_cvt_pk_bf16_f32 v7, v12, v13
	global_store_dwordx4 v[2:3], v[4:7], off offset:256
	v_mul_f32_e32 v10, 0x3b800000, v183
	v_pk_mul_f32 v[14:15], v[10:11], v[124:125] op_sel_hi:[0,1]
	v_or_b32_e32 v4, 16, v8
	v_ashrrev_i32_e32 v5, 31, v4
	v_lshlrev_b64 v[4:5], 12, v[4:5]
	v_lshl_add_u64 v[4:5], s[6:7], 0, v[4:5]
	v_lshl_add_u64 v[12:13], v[4:5], 0, v[154:155]
	v_pk_mul_f32 v[4:5], v[10:11], v[126:127] op_sel_hi:[0,1]
	v_pk_mul_f32 v[6:7], v[10:11], v[128:129] op_sel_hi:[0,1]
	v_cvt_pk_bf16_f32 v4, v4, v5
	v_cvt_pk_bf16_f32 v5, v6, v7
	v_pk_mul_f32 v[16:17], v[10:11], v[122:123] op_sel_hi:[0,1]
	v_cvt_pk_bf16_f32 v6, v16, v17
	v_cvt_pk_bf16_f32 v7, v14, v15
	global_store_dwordx4 v[12:13], v[4:7], off
	v_pk_mul_f32 v[14:15], v[10:11], v[116:117] op_sel_hi:[0,1]
	s_nop 0
	v_pk_mul_f32 v[4:5], v[10:11], v[118:119] op_sel_hi:[0,1]
	v_pk_mul_f32 v[6:7], v[10:11], v[120:121] op_sel_hi:[0,1]
	v_cvt_pk_bf16_f32 v4, v4, v5
	v_pk_mul_f32 v[10:11], v[10:11], v[114:115] op_sel_hi:[0,1]
	v_cvt_pk_bf16_f32 v5, v6, v7
	v_cvt_pk_bf16_f32 v6, v10, v11
	v_cvt_pk_bf16_f32 v7, v14, v15
	global_store_dwordx4 v[12:13], v[4:7], off offset:256
	v_mul_f32_e32 v10, 0x3b800000, v182
	v_pk_mul_f32 v[14:15], v[10:11], v[108:109] op_sel_hi:[0,1]
	v_or_b32_e32 v4, 32, v8
	v_ashrrev_i32_e32 v5, 31, v4
	v_lshlrev_b64 v[4:5], 12, v[4:5]
	v_lshl_add_u64 v[4:5], s[6:7], 0, v[4:5]
	v_lshl_add_u64 v[12:13], v[4:5], 0, v[154:155]
	v_pk_mul_f32 v[4:5], v[10:11], v[110:111] op_sel_hi:[0,1]
	v_pk_mul_f32 v[6:7], v[10:11], v[112:113] op_sel_hi:[0,1]
	v_cvt_pk_bf16_f32 v4, v4, v5
	v_cvt_pk_bf16_f32 v5, v6, v7
	v_pk_mul_f32 v[16:17], v[10:11], v[106:107] op_sel_hi:[0,1]
	v_cvt_pk_bf16_f32 v6, v16, v17
	v_cvt_pk_bf16_f32 v7, v14, v15
	global_store_dwordx4 v[12:13], v[4:7], off
	v_pk_mul_f32 v[14:15], v[10:11], v[100:101] op_sel_hi:[0,1]
	s_nop 0
	v_pk_mul_f32 v[4:5], v[10:11], v[102:103] op_sel_hi:[0,1]
	v_pk_mul_f32 v[6:7], v[10:11], v[104:105] op_sel_hi:[0,1]
	v_cvt_pk_bf16_f32 v4, v4, v5
	v_pk_mul_f32 v[10:11], v[10:11], v[98:99] op_sel_hi:[0,1]
	v_cvt_pk_bf16_f32 v5, v6, v7
	v_cvt_pk_bf16_f32 v6, v10, v11
	v_cvt_pk_bf16_f32 v7, v14, v15
	global_store_dwordx4 v[12:13], v[4:7], off offset:256
	s_nop 1
	v_or_b32_e32 v4, 48, v8
	v_ashrrev_i32_e32 v5, 31, v4
	v_lshlrev_b64 v[4:5], 12, v[4:5]
	v_mul_f32_e32 v8, 0x3b800000, v181
	v_lshl_add_u64 v[4:5], s[6:7], 0, v[4:5]
	v_lshl_add_u64 v[10:11], v[4:5], 0, v[154:155]
	v_pk_mul_f32 v[6:7], v[8:9], v[96:97] op_sel_hi:[0,1]
	v_pk_mul_f32 v[4:5], v[8:9], v[94:95] op_sel_hi:[0,1]
	v_pk_mul_f32 v[12:13], v[8:9], v[92:93] op_sel_hi:[0,1]
	v_pk_mul_f32 v[14:15], v[8:9], v[90:91] op_sel_hi:[0,1]
	v_cvt_pk_bf16_f32 v4, v4, v5
	v_cvt_pk_bf16_f32 v5, v6, v7
	v_cvt_pk_bf16_f32 v6, v14, v15
	v_cvt_pk_bf16_f32 v7, v12, v13
	global_store_dwordx4 v[10:11], v[4:7], off
	v_pk_mul_f32 v[12:13], v[8:9], v[84:85] op_sel_hi:[0,1]
	s_nop 0
	v_pk_mul_f32 v[6:7], v[8:9], v[88:89] op_sel_hi:[0,1]
	v_pk_mul_f32 v[4:5], v[8:9], v[86:87] op_sel_hi:[0,1]
	v_pk_mul_f32 v[8:9], v[8:9], v[82:83] op_sel_hi:[0,1]
	v_cvt_pk_bf16_f32 v4, v4, v5
	v_cvt_pk_bf16_f32 v5, v6, v7
	v_cvt_pk_bf16_f32 v6, v8, v9
	v_cvt_pk_bf16_f32 v7, v12, v13
	v_mul_f32_e32 v8, 0x3b800000, v180
	global_store_dwordx4 v[10:11], v[4:7], off offset:256
	v_pk_mul_f32 v[12:13], v[8:9], v[76:77] op_sel_hi:[0,1]
	v_pk_mul_f32 v[14:15], v[8:9], v[74:75] op_sel_hi:[0,1]
	v_pk_mul_f32 v[6:7], v[8:9], v[80:81] op_sel_hi:[0,1]
	v_pk_mul_f32 v[4:5], v[8:9], v[78:79] op_sel_hi:[0,1]
	v_cvt_pk_bf16_f32 v4, v4, v5
	v_cvt_pk_bf16_f32 v5, v6, v7
	v_cvt_pk_bf16_f32 v6, v14, v15
	v_cvt_pk_bf16_f32 v7, v12, v13
	v_add_co_u32_e32 v12, vcc, s52, v2
	v_lshl_add_u64 v[10:11], v[2:3], 0, s[10:11]
	s_nop 0
	v_addc_co_u32_e32 v13, vcc, 0, v3, vcc
	global_store_dwordx4 v[12:13], v[4:7], off
	v_pk_mul_f32 v[12:13], v[8:9], v[64:65] op_sel_hi:[0,1]
	s_nop 0
	v_pk_mul_f32 v[6:7], v[8:9], v[72:73] op_sel_hi:[0,1]
	v_pk_mul_f32 v[4:5], v[8:9], v[70:71] op_sel_hi:[0,1]
	v_pk_mul_f32 v[8:9], v[8:9], v[62:63] op_sel_hi:[0,1]
	v_cvt_pk_bf16_f32 v4, v4, v5
	v_cvt_pk_bf16_f32 v5, v6, v7
	v_cvt_pk_bf16_f32 v6, v8, v9
	v_cvt_pk_bf16_f32 v7, v12, v13
	v_mul_f32_e32 v8, 0x3b800000, v179
	global_store_dwordx4 v[10:11], v[4:7], off offset:256
	v_pk_mul_f32 v[12:13], v[8:9], v[60:61] op_sel_hi:[0,1]
	v_pk_mul_f32 v[14:15], v[8:9], v[58:59] op_sel_hi:[0,1]
	v_pk_mul_f32 v[6:7], v[8:9], v[68:69] op_sel_hi:[0,1]
	v_pk_mul_f32 v[4:5], v[8:9], v[66:67] op_sel_hi:[0,1]
	v_cvt_pk_bf16_f32 v4, v4, v5
	v_cvt_pk_bf16_f32 v5, v6, v7
	v_cvt_pk_bf16_f32 v6, v14, v15
	v_cvt_pk_bf16_f32 v7, v12, v13
	v_add_co_u32_e32 v12, vcc, s53, v2
	v_lshl_add_u64 v[10:11], v[2:3], 0, s[12:13]
	s_nop 0
	v_addc_co_u32_e32 v13, vcc, 0, v3, vcc
	global_store_dwordx4 v[12:13], v[4:7], off
	v_pk_mul_f32 v[12:13], v[8:9], v[48:49] op_sel_hi:[0,1]
	s_nop 0
	v_pk_mul_f32 v[6:7], v[8:9], v[56:57] op_sel_hi:[0,1]
	v_pk_mul_f32 v[4:5], v[8:9], v[54:55] op_sel_hi:[0,1]
	v_pk_mul_f32 v[8:9], v[8:9], v[46:47] op_sel_hi:[0,1]
	v_cvt_pk_bf16_f32 v4, v4, v5
	v_cvt_pk_bf16_f32 v5, v6, v7
	v_cvt_pk_bf16_f32 v6, v8, v9
	v_cvt_pk_bf16_f32 v7, v12, v13
	v_mul_f32_e32 v8, 0x3b800000, v173
	global_store_dwordx4 v[10:11], v[4:7], off offset:256
	v_pk_mul_f32 v[12:13], v[8:9], v[44:45] op_sel_hi:[0,1]
	v_pk_mul_f32 v[14:15], v[8:9], v[42:43] op_sel_hi:[0,1]
	v_pk_mul_f32 v[6:7], v[8:9], v[52:53] op_sel_hi:[0,1]
	v_pk_mul_f32 v[4:5], v[8:9], v[50:51] op_sel_hi:[0,1]
	v_cvt_pk_bf16_f32 v4, v4, v5
	v_cvt_pk_bf16_f32 v5, v6, v7
	v_cvt_pk_bf16_f32 v6, v14, v15
	v_cvt_pk_bf16_f32 v7, v12, v13
	v_add_co_u32_e32 v12, vcc, s54, v2
	v_lshl_add_u64 v[10:11], v[2:3], 0, s[14:15]
	s_nop 0
	v_addc_co_u32_e32 v13, vcc, 0, v3, vcc
	global_store_dwordx4 v[12:13], v[4:7], off
	v_pk_mul_f32 v[12:13], v[8:9], v[32:33] op_sel_hi:[0,1]
	s_nop 0
	v_pk_mul_f32 v[6:7], v[8:9], v[40:41] op_sel_hi:[0,1]
	v_pk_mul_f32 v[4:5], v[8:9], v[38:39] op_sel_hi:[0,1]
	v_pk_mul_f32 v[8:9], v[8:9], v[30:31] op_sel_hi:[0,1]
	v_cvt_pk_bf16_f32 v4, v4, v5
	v_cvt_pk_bf16_f32 v5, v6, v7
	v_cvt_pk_bf16_f32 v6, v8, v9
	v_mul_f32_e32 v8, 0x3b800000, v1
	v_cvt_pk_bf16_f32 v7, v12, v13
	global_store_dwordx4 v[10:11], v[4:7], off offset:256
	v_lshl_add_u64 v[10:11], v[2:3], 0, s[16:17]
	v_add_co_u32_e32 v2, vcc, s55, v2
	v_pk_mul_f32 v[4:5], v[8:9], v[34:35] op_sel_hi:[0,1]
	v_pk_mul_f32 v[6:7], v[8:9], v[36:37] op_sel_hi:[0,1]
	v_cvt_pk_bf16_f32 v4, v4, v5
	v_cvt_pk_bf16_f32 v5, v6, v7
	v_addc_co_u32_e32 v3, vcc, 0, v3, vcc
	v_pk_mul_f32 v[12:13], v[8:9], v[28:29] op_sel_hi:[0,1]
	v_pk_mul_f32 v[14:15], v[8:9], v[26:27] op_sel_hi:[0,1]
	v_cvt_pk_bf16_f32 v6, v14, v15
	v_cvt_pk_bf16_f32 v7, v12, v13
	global_store_dwordx4 v[2:3], v[4:7], off
	v_pk_mul_f32 v[2:3], v[8:9], v[22:23] op_sel_hi:[0,1]
	s_andn2_b64 vcc, exec, s[0:1]
	v_pk_mul_f32 v[4:5], v[8:9], v[24:25] op_sel_hi:[0,1]
	s_mov_b64 s[0:1], -1
	v_pk_mul_f32 v[6:7], v[8:9], v[20:21] op_sel_hi:[0,1]
	v_pk_mul_f32 v[8:9], v[8:9], v[18:19] op_sel_hi:[0,1]
	v_cvt_pk_bf16_f32 v2, v2, v3
	v_cvt_pk_bf16_f32 v3, v4, v5
	v_cvt_pk_bf16_f32 v4, v8, v9
	v_cvt_pk_bf16_f32 v5, v6, v7
	global_store_dwordx4 v[10:11], v[2:5], off offset:256
	s_cbranch_vccnz .LBB0_1120
	s_nop 0
	v_lshl_add_u32 v2, s18, 8, v172
	v_ashrrev_i32_e32 v3, 31, v2
	v_lshl_add_u64 v[2:3], v[2:3], 2, s[4:5]
	global_load_dword v154, v[2:3], off
	global_load_dword v183, v[2:3], off offset:64
	global_load_dword v182, v[2:3], off offset:128
	global_load_dword v181, v[2:3], off offset:192
	global_load_dword v180, v[2:3], off offset:512
	global_load_dword v179, v[2:3], off offset:576
	global_load_dword v173, v[2:3], off offset:640
	global_load_dword v1, v[2:3], off offset:704
	s_mov_b64 s[0:1], 0
	s_branch .LBB0_1120
